# first K iteration of each GEMM unit peeled: C=0 MFMAs replace accumulator zeroing, counted vmcnt past epilogue stores and prefetch (P8,P5), P1 ticket atomic wait deferred to K-loop end
# speedup vs baseline: 1.0200x; 1.0046x over previous
; #define PG8_STAGE(bufoff, gbase, voff) do { if constexpr (!(Sched::CRIP & 2)) _Pragma("unroll") for (int _i = 0; _i < 2; ++_i) { unsigned _o = (voff)[_i]; asm volatile("" : "+v"(_o)); \
;         __builtin_amdgcn_global_load_lds((const unsigned*)((const char*)(gbase) + _o), (LAS unsigned*)(lds + (bufoff) + ldsw + _i * 8192), 16, 0, 0); } } while (0)
; #define PG8_LDA(dst, b, h) do { if constexpr (!(Sched::CRIP & 4)) _Pragma("unroll") for (int m = 0; m < 4; ++m) dst[m] = PG8_CAT(*(const LAS i32x4*)(lds + PG8_SA(b, h) + aoff + m * 2048), *(const LAS i32x4*)(lds + PG8_SA(b, h) + aoff + m * 2048 + 1024)); } while (0)
; #define PG8_LDB(dst, b, h) do { if constexpr (!(Sched::CRIP & 4)) _Pragma("unroll") for (int n = 0; n < 2; ++n) dst[n] = PG8_CAT(*(const LAS i32x4*)(lds + PG8_SB(b, h) + boff + n * 2048), *(const LAS i32x4*)(lds + PG8_SB(b, h) + boff + n * 2048 + 1024)); } while (0)
; #define PG8_WAIT_V(n) asm volatile("s_waitcnt vmcnt(" #n ")" ::: "memory")
; #define PG8_WAIT_L(n) asm volatile("s_waitcnt lgkmcnt(" #n ")" ::: "memory")
; #define PG8_BAR __builtin_amdgcn_s_barrier()
; #define PG8_SCHED __builtin_amdgcn_sched_barrier(0)
; template <class Epi, class Sched>
; __device__ __forceinline__ void gemm_phase(LAS unsigned char* lds, const Sched& S, const Epi& E) {
;     ...
;             PG8_LDB(B0, 0, 0); PG8_LDB(B1, 0, 1); PG8_SCHED; PG8_LDA(At, 0, 0); PG8_STAGE(PG8_SA(1, 1), a1, vA[1]);
;             PG8_WAIT_V(8); PG8_WAIT_L(0); PG8_BAR; PG8_MMA(0, 0, At, B0); PG8_MMA(0, 1, At, B1); PG8_BAR2; PG8_SCHED;
;     __device__ __forceinline__ bool next(int i, Unit& u) const {
;         const int t = __builtin_amdgcn_readfirstlane(tk[i & 1]);
;         if (i > 0 && threadIdx.x == 0) tk[(i + 1) & 1] = (int)__hip_atomic_fetch_add(tick, 1u, __ATOMIC_RELAXED, __HIP_MEMORY_SCOPE_AGENT);
;         if (t >= q) return false;
;         const int id = xcd * q + t, nig = WGMQ * nN, gid = id / nig, fm = gid * WGMQ, gsz = (nM - fm) < WGMQ ? (nM - fm) : WGMQ;
;         const int pm = fm + ((id % nig) % gsz), pn = (id % nig) / gsz;
;         u.pm = pm; u.pn = pn; u.e = 0; u.aidx = nullptr; u.avalid = 256;
;         u.aBase = A + (size_t)pm * 256 * ROWB; u.bBase = Bt + (size_t)pn * 256 * ROWB; return true;
.LBB0_204:
	s_add_i32 s74, s74, 1
	s_and_b32 s25, s74, 1
	s_lshl_b32 s17, s25, 2
	s_add_i32 s17, s17, 0
	s_add_i32 s17, s17, 0x27f00
	v_mov_b32_e32 v2, s17
	ds_read_b32 v2, v2
	s_waitcnt lgkmcnt(0)
	v_readfirstlane_b32 s17, v2
	s_and_saveexec_b64 s[18:19], s[0:1]
	s_cbranch_execz .LBB0_208
	s_mov_b64 s[22:23], exec
	v_mbcnt_lo_u32_b32 v247, s22, 0
	v_mbcnt_hi_u32_b32 v247, s23, v247
	v_cmp_eq_u32_e32 vcc, 0, v247
	s_and_saveexec_b64 s[20:21], vcc
	s_cbranch_execz .LBB0_207
	s_bcnt1_i32_b64 s22, s[22:23]
	v_mov_b32_e32 v246, s22
	global_atomic_add v246, v131, v246, s[6:7] sc0
.LBB0_207:
	s_or_b64 exec, exec, s[20:21]
.LBB0_208:
	s_or_b64 exec, exec, s[18:19]
	s_cmpk_lt_i32 s17, 0x100
	s_cselect_b64 s[20:21], -1, 0
	s_cmpk_gt_i32 s17, 0xff
	s_mov_b64 s[22:23], s[28:29]
	s_mov_b64 s[18:19], s[26:27]
	s_cbranch_scc1 .LBB0_210
	s_add_i32 s16, s17, s2
	s_ashr_i32 s17, s16, 31
	s_lshr_b32 s17, s17, 25
	s_add_i32 s17, s16, s17
	s_ashr_i32 s18, s17, 7
	s_and_b32 s17, s17, 0xff80
	s_sub_i32 s16, s16, s17
	s_bfe_i32 s17, s16, 0x80000
	s_bfe_u32 s17, s17, 0x3000c
	s_add_i32 s17, s16, s17
	s_and_b32 s19, s17, 0xf8
	s_sub_i32 s16, s16, s19
	s_lshl_b32 s18, s18, 3
	s_sext_i32_i8 s16, s16
	s_bfe_i32 s17, s17, 0x80000
	s_add_i32 s16, s18, s16
	s_sext_i32_i16 s17, s17
	s_lshr_b32 s22, s17, 3
	s_ashr_i32 s91, s17, 3
	s_ashr_i32 s17, s16, 31
	s_lshl_b64 s[18:19], s[16:17], 20
	s_add_u32 s18, s38, s18
	s_addc_u32 s19, s42, s19
	s_bfe_i64 s[22:23], s[22:23], 0x100000
	s_lshl_b64 s[22:23], s[22:23], 20
	s_add_u32 s22, s43, s22
	s_addc_u32 s23, s46, s23
.LBB0_210:
	s_add_i32 s17, s16, s91
	s_and_b32 s17, s17, 31
	s_and_b64 s[34:35], s[20:21], exec
	s_cselect_b32 s25, s17, s30
	s_lshl_b32 s31, s25, 7
	s_add_u32 s25, s18, s31
	s_addc_u32 s39, s19, 0
	s_add_u32 s40, s22, s31
	s_addc_u32 s41, s23, 0
	s_addk_i32 s31, 0x80
	s_and_b32 s31, s31, 0xf80
	s_add_u32 s44, s18, s31
	s_addc_u32 s45, s19, 0
	s_add_u32 s48, s22, s31
	s_addc_u32 s49, s23, 0
	s_lshl_b32 s30, s30, 7
	s_add_i32 s52, s30, 0x180
	s_mov_b32 s53, -2
	s_add_i32 s30, s52, 0xffffff00
	s_add_i32 s31, s52, 0xffffff80
	s_and_b32 s30, s30, 0xf80
	s_and_b32 s31, s31, 0xf80
	s_add_u32 s34, s26, s31
	s_addc_u32 s35, s27, 0
	s_add_u32 s54, s28, s31
	s_addc_u32 s55, s29, 0
	s_and_b32 s31, s52, 0xf80
	s_add_u32 s92, s26, s31
	s_addc_u32 s93, s27, 0
	ds_read_b128 v[144:147], v140
	ds_read_b128 v[148:151], v140 offset:1024
	ds_read_b128 v[152:155], v140 offset:2048
	ds_read_b128 v[156:159], v140 offset:3072
	ds_read_b128 v[160:163], v141
	ds_read_b128 v[164:167], v141 offset:1024
	ds_read_b128 v[168:171], v141 offset:2048
	ds_read_b128 v[172:175], v141 offset:3072
	s_add_u32 s94, s28, s31
	s_addc_u32 s95, s29, 0
	s_add_u32 s36, s26, s30
	s_addc_u32 s37, s27, 0
	s_add_i32 vcc_lo, s75, s47
	s_add_i32 m0, s50, 0xc000
	s_add_i32 s97, s50, 0xe000
	s_add_i32 vcc_hi, vcc_lo, 0x2000
	s_cmp_eq_u32 s53, 28
	s_cselect_b32 s35, s39, s35
	s_cselect_b32 s34, s25, s34
	s_cselect_b32 s31, s45, s93
	s_cselect_b32 s30, s44, s92
	s_cselect_b32 s55, s41, s55
	s_cselect_b32 s54, s40, s54
	v_mov_b32_e32 v130, v137
	ds_read_b128 v[176:179], v142
	ds_read_b128 v[180:183], v142 offset:1024
	ds_read_b128 v[184:187], v142 offset:2048
	ds_read_b128 v[188:191], v142 offset:3072
	ds_read_b128 v[192:195], v142 offset:4096
	ds_read_b128 v[196:199], v142 offset:5120
	ds_read_b128 v[200:203], v142 offset:6144
	ds_read_b128 v[204:207], v142 offset:7168
	s_nop 0
	global_load_lds_dwordx4 v130, s[36:37]
	v_mov_b32_e32 v130, v138
	s_mov_b32 m0, s97
	s_nop 0
	global_load_lds_dwordx4 v130, s[36:37]
	s_waitcnt vmcnt(8)
	s_waitcnt lgkmcnt(0)
	s_barrier
	s_setprio 1
	s_waitcnt lgkmcnt(0)
	v_mfma_f32_16x16x32_bf16 v[126:129], v[144:147], v[176:179], 0
	v_mfma_f32_16x16x32_bf16 v[122:125], v[152:155], v[176:179], 0
	v_mfma_f32_16x16x32_bf16 v[118:121], v[144:147], v[184:187], 0
	v_mfma_f32_16x16x32_bf16 v[114:117], v[152:155], v[184:187], 0
	v_mfma_f32_16x16x32_bf16 v[102:105], v[144:147], v[192:195], 0
	v_mfma_f32_16x16x32_bf16 v[98:101], v[152:155], v[192:195], 0
	v_mfma_f32_16x16x32_bf16 v[86:89], v[144:147], v[200:203], 0
	v_mfma_f32_16x16x32_bf16 v[82:85], v[152:155], v[200:203], 0
	v_mfma_f32_16x16x32_bf16 v[126:129], v[148:151], v[180:183], v[126:129]
	v_mfma_f32_16x16x32_bf16 v[122:125], v[156:159], v[180:183], v[122:125]
	v_mfma_f32_16x16x32_bf16 v[118:121], v[148:151], v[188:191], v[118:121]
	v_mfma_f32_16x16x32_bf16 v[114:117], v[156:159], v[188:191], v[114:117]
	v_mfma_f32_16x16x32_bf16 v[102:105], v[148:151], v[196:199], v[102:105]
	v_mfma_f32_16x16x32_bf16 v[98:101], v[156:159], v[196:199], v[98:101]
	v_mfma_f32_16x16x32_bf16 v[86:89], v[148:151], v[204:207], v[86:89]
	v_mfma_f32_16x16x32_bf16 v[82:85], v[156:159], v[204:207], v[82:85]
	s_setprio 0
	s_setprio 1
	v_mfma_f32_16x16x32_bf16 v[110:113], v[160:163], v[176:179], 0
	v_mfma_f32_16x16x32_bf16 v[106:109], v[168:171], v[176:179], 0
	v_mfma_f32_16x16x32_bf16 v[94:97], v[160:163], v[184:187], 0
	v_mfma_f32_16x16x32_bf16 v[90:93], v[168:171], v[184:187], 0
	v_mfma_f32_16x16x32_bf16 v[78:81], v[160:163], v[192:195], 0
	v_mfma_f32_16x16x32_bf16 v[74:77], v[168:171], v[192:195], 0
	v_mfma_f32_16x16x32_bf16 v[70:73], v[160:163], v[200:203], 0
	v_mfma_f32_16x16x32_bf16 v[66:69], v[168:171], v[200:203], 0
	v_mfma_f32_16x16x32_bf16 v[110:113], v[164:167], v[180:183], v[110:113]
	v_mfma_f32_16x16x32_bf16 v[106:109], v[172:175], v[180:183], v[106:109]
	v_mfma_f32_16x16x32_bf16 v[94:97], v[164:167], v[188:191], v[94:97]
	v_mfma_f32_16x16x32_bf16 v[90:93], v[172:175], v[188:191], v[90:93]
	v_mfma_f32_16x16x32_bf16 v[78:81], v[164:167], v[196:199], v[78:81]
	v_mfma_f32_16x16x32_bf16 v[74:77], v[172:175], v[196:199], v[74:77]
	v_mfma_f32_16x16x32_bf16 v[70:73], v[164:167], v[204:207], v[70:73]
	v_mfma_f32_16x16x32_bf16 v[66:69], v[172:175], v[204:207], v[66:69]
	s_setprio 0
	s_barrier
; #define PG8_STAGE(bufoff, gbase, voff) do { if constexpr (!(Sched::CRIP & 2)) _Pragma("unroll") for (int _i = 0; _i < 2; ++_i) { unsigned _o = (voff)[_i]; asm volatile("" : "+v"(_o)); \
;         __builtin_amdgcn_global_load_lds((const unsigned*)((const char*)(gbase) + _o), (LAS unsigned*)(lds + (bufoff) + ldsw + _i * 8192), 16, 0, 0); } } while (0)
; #define PG8_LDA(dst, b, h) do { if constexpr (!(Sched::CRIP & 4)) _Pragma("unroll") for (int m = 0; m < 4; ++m) dst[m] = PG8_CAT(*(const LAS i32x4*)(lds + PG8_SA(b, h) + aoff + m * 2048), *(const LAS i32x4*)(lds + PG8_SA(b, h) + aoff + m * 2048 + 1024)); } while (0)
; #define PG8_LDB(dst, b, h) do { if constexpr (!(Sched::CRIP & 4)) _Pragma("unroll") for (int n = 0; n < 2; ++n) dst[n] = PG8_CAT(*(const LAS i32x4*)(lds + PG8_SB(b, h) + boff + n * 2048), *(const LAS i32x4*)(lds + PG8_SB(b, h) + boff + n * 2048 + 1024)); } while (0)
; #define PG8_WAIT_V(n) asm volatile("s_waitcnt vmcnt(" #n ")" ::: "memory")
; #define PG8_WAIT_L(n) asm volatile("s_waitcnt lgkmcnt(" #n ")" ::: "memory")
; #define PG8_BAR __builtin_amdgcn_s_barrier()
; #define PG8_SCHED __builtin_amdgcn_sched_barrier(0)
; template <class Epi, class Sched>
; __device__ __forceinline__ void gemm_phase(LAS unsigned char* lds, const Sched& S, const Epi& E) {
;     ...
;             PG8_LDA(At, 0, 1); PG8_STAGE(PG8_SB(0, 0), b2, voffB); PG8_STAGE(PG8_SB(0, 1), b2 + hstep, voffB); PG8_STAGE(PG8_SA(0, 0), a2, vA[0]);
;             PG8_WAIT_V(8); PG8_WAIT_L(0); PG8_BAR; PG8_MMA(1, 0, At, B0); PG8_MMA(1, 1, At, B1); PG8_BAR2; PG8_SCHED;
;             PG8_LDB(B0, 1, 0); PG8_LDB(B1, 1, 1); PG8_SCHED; PG8_LDA(At, 1, 0); PG8_STAGE(PG8_SA(0, 1), a2, vA[1]);
;             PG8_WAIT_V(8); PG8_WAIT_L(0); PG8_BAR; PG8_MMA(0, 0, At, B0); PG8_MMA(0, 1, At, B1); PG8_BAR2; PG8_SCHED;
	v_mov_b32_e32 v130, v1
	s_mov_b32 m0, vcc_lo
	ds_read_b128 v[176:179], v142 offset:16384
	ds_read_b128 v[180:183], v142 offset:17408
	ds_read_b128 v[184:187], v142 offset:18432
	ds_read_b128 v[188:191], v142 offset:19456
	ds_read_b128 v[192:195], v142 offset:20480
	ds_read_b128 v[196:199], v142 offset:21504
	ds_read_b128 v[200:203], v142 offset:22528
	ds_read_b128 v[204:207], v142 offset:23552
	s_cselect_b32 s36, s48, s94
	global_load_lds_dwordx4 v130, s[54:55]
	v_mov_b32_e32 v130, v134
	s_mov_b32 m0, vcc_hi
	s_cselect_b32 s37, s49, s95
	global_load_lds_dwordx4 v130, s[54:55]
	s_add_u32 s54, s54, 0x80000
	v_mov_b32_e32 v130, v1
	s_addc_u32 s55, s55, 0
	s_add_i32 s92, s76, s47
	s_mov_b32 m0, s92
	s_nop 0
	global_load_lds_dwordx4 v130, s[54:55]
	v_mov_b32_e32 v130, v134
	s_add_i32 m0, s92, 0x2000
	s_nop 0
	global_load_lds_dwordx4 v130, s[54:55]
	v_mov_b32_e32 v130, v135
	s_mov_b32 m0, s50
	s_nop 0
	global_load_lds_dwordx4 v130, s[34:35]
	v_mov_b32_e32 v130, v136
	s_mov_b32 m0, s51
	s_nop 0
	global_load_lds_dwordx4 v130, s[34:35]
	s_waitcnt vmcnt(8)
	s_waitcnt lgkmcnt(0)
	s_barrier
	s_setprio 1
	s_waitcnt lgkmcnt(0)
	v_mfma_f32_16x16x32_bf16 v[62:65], v[144:147], v[176:179], 0
	v_mfma_f32_16x16x32_bf16 v[58:61], v[152:155], v[176:179], 0
	v_mfma_f32_16x16x32_bf16 v[54:57], v[144:147], v[184:187], 0
	v_mfma_f32_16x16x32_bf16 v[50:53], v[152:155], v[184:187], 0
	v_mfma_f32_16x16x32_bf16 v[38:41], v[144:147], v[192:195], 0
	v_mfma_f32_16x16x32_bf16 v[34:37], v[152:155], v[192:195], 0
	v_mfma_f32_16x16x32_bf16 v[22:25], v[144:147], v[200:203], 0
	v_mfma_f32_16x16x32_bf16 v[18:21], v[152:155], v[200:203], 0
	v_mfma_f32_16x16x32_bf16 v[62:65], v[148:151], v[180:183], v[62:65]
	v_mfma_f32_16x16x32_bf16 v[58:61], v[156:159], v[180:183], v[58:61]
	v_mfma_f32_16x16x32_bf16 v[54:57], v[148:151], v[188:191], v[54:57]
	v_mfma_f32_16x16x32_bf16 v[50:53], v[156:159], v[188:191], v[50:53]
	v_mfma_f32_16x16x32_bf16 v[38:41], v[148:151], v[196:199], v[38:41]
	v_mfma_f32_16x16x32_bf16 v[34:37], v[156:159], v[196:199], v[34:37]
	v_mfma_f32_16x16x32_bf16 v[22:25], v[148:151], v[204:207], v[22:25]
	v_mfma_f32_16x16x32_bf16 v[18:21], v[156:159], v[204:207], v[18:21]
	s_setprio 0
	s_setprio 1
	v_mfma_f32_16x16x32_bf16 v[46:49], v[160:163], v[176:179], 0
	v_mfma_f32_16x16x32_bf16 v[42:45], v[168:171], v[176:179], 0
	v_mfma_f32_16x16x32_bf16 v[30:33], v[160:163], v[184:187], 0
	v_mfma_f32_16x16x32_bf16 v[26:29], v[168:171], v[184:187], 0
	v_mfma_f32_16x16x32_bf16 v[14:17], v[160:163], v[192:195], 0
	v_mfma_f32_16x16x32_bf16 v[10:13], v[168:171], v[192:195], 0
	v_mfma_f32_16x16x32_bf16 v[6:9], v[160:163], v[200:203], 0
	v_mfma_f32_16x16x32_bf16 v[2:5], v[168:171], v[200:203], 0
	v_mfma_f32_16x16x32_bf16 v[46:49], v[164:167], v[180:183], v[46:49]
	v_mfma_f32_16x16x32_bf16 v[42:45], v[172:175], v[180:183], v[42:45]
	v_mfma_f32_16x16x32_bf16 v[30:33], v[164:167], v[188:191], v[30:33]
	v_mfma_f32_16x16x32_bf16 v[26:29], v[172:175], v[188:191], v[26:29]
	v_mfma_f32_16x16x32_bf16 v[14:17], v[164:167], v[196:199], v[14:17]
	v_mfma_f32_16x16x32_bf16 v[10:13], v[172:175], v[196:199], v[10:13]
	v_mfma_f32_16x16x32_bf16 v[6:9], v[164:167], v[204:207], v[6:9]
	v_mfma_f32_16x16x32_bf16 v[2:5], v[172:175], v[204:207], v[2:5]
	s_setprio 0
	s_barrier
	s_add_i32 s54, 0, 0x18000
	v_add_u32_e32 v130, s54, v139
	s_add_i32 s55, 0, 0x1c000
	ds_read_b128 v[144:147], v130
	ds_read_b128 v[148:151], v130 offset:1024
	ds_read_b128 v[152:155], v130 offset:2048
	ds_read_b128 v[156:159], v130 offset:3072
	v_add_u32_e32 v130, s55, v139
	ds_read_b128 v[160:163], v130
	ds_read_b128 v[164:167], v130 offset:1024
	ds_read_b128 v[168:171], v130 offset:2048
	ds_read_b128 v[172:175], v130 offset:3072
	v_mov_b32_e32 v130, v137
	s_mov_b32 m0, s66
	ds_read_b128 v[176:179], v142 offset:32768
	ds_read_b128 v[180:183], v142 offset:33792
	ds_read_b128 v[184:187], v142 offset:34816
	ds_read_b128 v[188:191], v142 offset:35840
	ds_read_b128 v[192:195], v142 offset:36864
	ds_read_b128 v[196:199], v142 offset:37888
	ds_read_b128 v[200:203], v142 offset:38912
	ds_read_b128 v[204:207], v142 offset:39936
	s_nop 0
	global_load_lds_dwordx4 v130, s[34:35]
	v_mov_b32_e32 v130, v138
	s_mov_b32 m0, s67
	s_nop 0
	global_load_lds_dwordx4 v130, s[34:35]
	s_waitcnt vmcnt(8)
	s_waitcnt lgkmcnt(0)
	s_barrier
	s_setprio 1
	s_waitcnt lgkmcnt(0)
	v_mfma_f32_16x16x32_bf16 v[126:129], v[144:147], v[176:179], v[126:129]
	v_mfma_f32_16x16x32_bf16 v[122:125], v[152:155], v[176:179], v[122:125]
	v_mfma_f32_16x16x32_bf16 v[118:121], v[144:147], v[184:187], v[118:121]
	v_mfma_f32_16x16x32_bf16 v[114:117], v[152:155], v[184:187], v[114:117]
	v_mfma_f32_16x16x32_bf16 v[102:105], v[144:147], v[192:195], v[102:105]
	v_mfma_f32_16x16x32_bf16 v[98:101], v[152:155], v[192:195], v[98:101]
	v_mfma_f32_16x16x32_bf16 v[86:89], v[144:147], v[200:203], v[86:89]
	v_mfma_f32_16x16x32_bf16 v[82:85], v[152:155], v[200:203], v[82:85]
	v_mfma_f32_16x16x32_bf16 v[126:129], v[148:151], v[180:183], v[126:129]
	v_mfma_f32_16x16x32_bf16 v[122:125], v[156:159], v[180:183], v[122:125]
	v_mfma_f32_16x16x32_bf16 v[118:121], v[148:151], v[188:191], v[118:121]
	v_mfma_f32_16x16x32_bf16 v[114:117], v[156:159], v[188:191], v[114:117]
	v_mfma_f32_16x16x32_bf16 v[102:105], v[148:151], v[196:199], v[102:105]
	v_mfma_f32_16x16x32_bf16 v[98:101], v[156:159], v[196:199], v[98:101]
	v_mfma_f32_16x16x32_bf16 v[86:89], v[148:151], v[204:207], v[86:89]
	v_mfma_f32_16x16x32_bf16 v[82:85], v[156:159], v[204:207], v[82:85]
	s_setprio 0
	s_setprio 1
	v_mfma_f32_16x16x32_bf16 v[110:113], v[160:163], v[176:179], v[110:113]
	v_mfma_f32_16x16x32_bf16 v[106:109], v[168:171], v[176:179], v[106:109]
	v_mfma_f32_16x16x32_bf16 v[94:97], v[160:163], v[184:187], v[94:97]
	v_mfma_f32_16x16x32_bf16 v[90:93], v[168:171], v[184:187], v[90:93]
	v_mfma_f32_16x16x32_bf16 v[78:81], v[160:163], v[192:195], v[78:81]
	v_mfma_f32_16x16x32_bf16 v[74:77], v[168:171], v[192:195], v[74:77]
	v_mfma_f32_16x16x32_bf16 v[70:73], v[160:163], v[200:203], v[70:73]
	v_mfma_f32_16x16x32_bf16 v[66:69], v[168:171], v[200:203], v[66:69]
	v_mfma_f32_16x16x32_bf16 v[110:113], v[164:167], v[180:183], v[110:113]
	v_mfma_f32_16x16x32_bf16 v[106:109], v[172:175], v[180:183], v[106:109]
	v_mfma_f32_16x16x32_bf16 v[94:97], v[164:167], v[188:191], v[94:97]
	v_mfma_f32_16x16x32_bf16 v[90:93], v[172:175], v[188:191], v[90:93]
	v_mfma_f32_16x16x32_bf16 v[78:81], v[164:167], v[196:199], v[78:81]
	v_mfma_f32_16x16x32_bf16 v[74:77], v[172:175], v[196:199], v[74:77]
	v_mfma_f32_16x16x32_bf16 v[70:73], v[164:167], v[204:207], v[70:73]
	v_mfma_f32_16x16x32_bf16 v[66:69], v[172:175], v[204:207], v[66:69]
	s_setprio 0
	s_barrier
; #define PG8_STAGE(bufoff, gbase, voff) do { if constexpr (!(Sched::CRIP & 2)) _Pragma("unroll") for (int _i = 0; _i < 2; ++_i) { unsigned _o = (voff)[_i]; asm volatile("" : "+v"(_o)); \
;         __builtin_amdgcn_global_load_lds((const unsigned*)((const char*)(gbase) + _o), (LAS unsigned*)(lds + (bufoff) + ldsw + _i * 8192), 16, 0, 0); } } while (0)
; #define PG8_LDA(dst, b, h) do { if constexpr (!(Sched::CRIP & 4)) _Pragma("unroll") for (int m = 0; m < 4; ++m) dst[m] = PG8_CAT(*(const LAS i32x4*)(lds + PG8_SA(b, h) + aoff + m * 2048), *(const LAS i32x4*)(lds + PG8_SA(b, h) + aoff + m * 2048 + 1024)); } while (0)
; #define PG8_LDB(dst, b, h) do { if constexpr (!(Sched::CRIP & 4)) _Pragma("unroll") for (int n = 0; n < 2; ++n) dst[n] = PG8_CAT(*(const LAS i32x4*)(lds + PG8_SB(b, h) + boff + n * 2048), *(const LAS i32x4*)(lds + PG8_SB(b, h) + boff + n * 2048 + 1024)); } while (0)
; #define PG8_WAIT_V(n) asm volatile("s_waitcnt vmcnt(" #n ")" ::: "memory")
; #define PG8_WAIT_L(n) asm volatile("s_waitcnt lgkmcnt(" #n ")" ::: "memory")
; #define PG8_BAR __builtin_amdgcn_s_barrier()
; #define PG8_SCHED __builtin_amdgcn_sched_barrier(0)
; template <class Epi, class Sched>
; __device__ __forceinline__ void gemm_phase(LAS unsigned char* lds, const Sched& S, const Epi& E) {
;     ...
;         for (int t = 0; t < nt; t += 2) {
;             const bool last = (t == nt - 2);
;             const char* a1 = cA + PG8_KT(crot, t + 1);
;             const char* a2 = last ? nA + PG8_KT(nrot, 0) : cA + PG8_KT(crot, t + 2); const char* b2 = last ? nB + PG8_KT(nrot, 0) : cB + PG8_KT(crot, t + 2);
;             const char* a3 = last ? nA + PG8_KT(nrot, 1) : cA + PG8_KT(crot, t + 3); const char* b3 = last ? nB + PG8_KT(nrot, 1) : cB + PG8_KT(crot, t + 3);
;             int gi = 0;
;             if constexpr (Sched::GATHER) { if (t == 0 && has_next && tid < 256) gi = nxt.aidx[tid]; }
;             PG8_LDB(B0, 0, 0); PG8_LDB(B1, 0, 1); PG8_SCHED; PG8_LDA(At, 0, 0); PG8_STAGE(PG8_SA(1, 1), a1, vA[1]);
;             PG8_WAIT_V(8); PG8_WAIT_L(0); PG8_BAR; PG8_MMA(0, 0, At, B0); PG8_MMA(0, 1, At, B1); PG8_BAR2; PG8_SCHED;
;     ...
;             PG8_LDA(At, 1, 1); PG8_STAGE(PG8_SB(1, 0), b3, voffB); PG8_STAGE(PG8_SB(1, 1), b3 + hstep, voffB); PG8_STAGE(PG8_SA(1, 0), a3, vA[0]);
;             PG8_WAIT_V(8); PG8_WAIT_L(0); PG8_BAR; PG8_MMA(1, 0, At, B0); PG8_MMA(1, 1, At, B1); PG8_BAR2; PG8_SCHED;
	v_mov_b32_e32 v130, v1
	s_add_i32 s34, s54, s47
	ds_read_b128 v[176:179], v142 offset:49152
	ds_read_b128 v[180:183], v142 offset:50176
	ds_read_b128 v[184:187], v142 offset:51200
	ds_read_b128 v[188:191], v142 offset:52224
	ds_read_b128 v[192:195], v142 offset:53248
	ds_read_b128 v[196:199], v142 offset:54272
	ds_read_b128 v[200:203], v142 offset:55296
	ds_read_b128 v[204:207], v142 offset:56320
	s_mov_b32 m0, s34
	s_nop 0
	global_load_lds_dwordx4 v130, s[36:37]
	v_mov_b32_e32 v130, v134
	s_add_i32 m0, s34, 0x2000
	s_add_u32 s34, s36, 0x80000
	global_load_lds_dwordx4 v130, s[36:37]
	s_addc_u32 s35, s37, 0
	v_mov_b32_e32 v130, v1
	s_add_i32 s36, s55, s47
	s_mov_b32 m0, s36
	s_nop 0
	global_load_lds_dwordx4 v130, s[34:35]
	v_mov_b32_e32 v130, v134
	s_add_i32 m0, s36, 0x2000
	s_nop 0
	global_load_lds_dwordx4 v130, s[34:35]
	v_mov_b32_e32 v130, v135
	s_mov_b32 m0, s70
	s_nop 0
	global_load_lds_dwordx4 v130, s[30:31]
	v_mov_b32_e32 v130, v136
	s_mov_b32 m0, s71
	s_nop 0
	global_load_lds_dwordx4 v130, s[30:31]
	s_waitcnt vmcnt(8)
	s_waitcnt lgkmcnt(0)
	s_barrier
	s_setprio 1
	s_waitcnt lgkmcnt(0)
	v_mfma_f32_16x16x32_bf16 v[62:65], v[144:147], v[176:179], v[62:65]
	v_mfma_f32_16x16x32_bf16 v[58:61], v[152:155], v[176:179], v[58:61]
	v_mfma_f32_16x16x32_bf16 v[54:57], v[144:147], v[184:187], v[54:57]
	v_mfma_f32_16x16x32_bf16 v[50:53], v[152:155], v[184:187], v[50:53]
	v_mfma_f32_16x16x32_bf16 v[38:41], v[144:147], v[192:195], v[38:41]
	v_mfma_f32_16x16x32_bf16 v[34:37], v[152:155], v[192:195], v[34:37]
	v_mfma_f32_16x16x32_bf16 v[22:25], v[144:147], v[200:203], v[22:25]
	v_mfma_f32_16x16x32_bf16 v[18:21], v[152:155], v[200:203], v[18:21]
	v_mfma_f32_16x16x32_bf16 v[62:65], v[148:151], v[180:183], v[62:65]
	v_mfma_f32_16x16x32_bf16 v[58:61], v[156:159], v[180:183], v[58:61]
	v_mfma_f32_16x16x32_bf16 v[54:57], v[148:151], v[188:191], v[54:57]
	v_mfma_f32_16x16x32_bf16 v[50:53], v[156:159], v[188:191], v[50:53]
	v_mfma_f32_16x16x32_bf16 v[38:41], v[148:151], v[196:199], v[38:41]
	v_mfma_f32_16x16x32_bf16 v[34:37], v[156:159], v[196:199], v[34:37]
	v_mfma_f32_16x16x32_bf16 v[22:25], v[148:151], v[204:207], v[22:25]
	v_mfma_f32_16x16x32_bf16 v[18:21], v[156:159], v[204:207], v[18:21]
	s_setprio 0
	s_setprio 1
	v_mfma_f32_16x16x32_bf16 v[46:49], v[160:163], v[176:179], v[46:49]
	v_mfma_f32_16x16x32_bf16 v[42:45], v[168:171], v[176:179], v[42:45]
	v_mfma_f32_16x16x32_bf16 v[30:33], v[160:163], v[184:187], v[30:33]
	v_mfma_f32_16x16x32_bf16 v[26:29], v[168:171], v[184:187], v[26:29]
	v_mfma_f32_16x16x32_bf16 v[14:17], v[160:163], v[192:195], v[14:17]
	v_mfma_f32_16x16x32_bf16 v[10:13], v[168:171], v[192:195], v[10:13]
	v_mfma_f32_16x16x32_bf16 v[6:9], v[160:163], v[200:203], v[6:9]
	v_mfma_f32_16x16x32_bf16 v[2:5], v[168:171], v[200:203], v[2:5]
	v_mfma_f32_16x16x32_bf16 v[46:49], v[164:167], v[180:183], v[46:49]
	v_mfma_f32_16x16x32_bf16 v[42:45], v[172:175], v[180:183], v[42:45]
	v_mfma_f32_16x16x32_bf16 v[30:33], v[164:167], v[188:191], v[30:33]
	v_mfma_f32_16x16x32_bf16 v[26:29], v[172:175], v[188:191], v[26:29]
	v_mfma_f32_16x16x32_bf16 v[14:17], v[164:167], v[196:199], v[14:17]
	v_mfma_f32_16x16x32_bf16 v[10:13], v[172:175], v[196:199], v[10:13]
	v_mfma_f32_16x16x32_bf16 v[6:9], v[164:167], v[204:207], v[6:9]
	v_mfma_f32_16x16x32_bf16 v[2:5], v[172:175], v[204:207], v[2:5]
	s_setprio 0
	s_barrier
	s_add_i32 s53, s53, 2
	s_addk_i32 s52, 0x100
.LBB0_211:
	s_add_i32 s30, s52, 0xffffff00
	s_add_i32 s31, s52, 0xffffff80
	s_and_b32 s30, s30, 0xf80
	s_and_b32 s31, s31, 0xf80
	s_add_u32 s34, s26, s31
	s_addc_u32 s35, s27, 0
	s_add_u32 s54, s28, s31
	s_addc_u32 s55, s29, 0
	s_and_b32 s31, s52, 0xf80
	s_add_u32 s92, s26, s31
	s_addc_u32 s93, s27, 0
	ds_read_b128 v[144:147], v140
	ds_read_b128 v[148:151], v140 offset:1024
	ds_read_b128 v[152:155], v140 offset:2048
	ds_read_b128 v[156:159], v140 offset:3072
	ds_read_b128 v[160:163], v141
	ds_read_b128 v[164:167], v141 offset:1024
	ds_read_b128 v[168:171], v141 offset:2048
	ds_read_b128 v[172:175], v141 offset:3072
	s_add_u32 s94, s28, s31
	s_addc_u32 s95, s29, 0
	s_add_u32 s36, s26, s30
	s_addc_u32 s37, s27, 0
	s_add_i32 vcc_lo, s75, s47
	s_add_i32 m0, s50, 0xc000
	s_add_i32 s97, s50, 0xe000
	s_add_i32 vcc_hi, vcc_lo, 0x2000
	s_cmp_eq_u32 s53, 28
	s_cselect_b32 s35, s39, s35
	s_cselect_b32 s34, s25, s34
	s_cselect_b32 s31, s45, s93
	s_cselect_b32 s30, s44, s92
	s_cselect_b32 s55, s41, s55
	s_cselect_b32 s54, s40, s54
	v_mov_b32_e32 v130, v137
	ds_read_b128 v[176:179], v142
	ds_read_b128 v[180:183], v142 offset:1024
	ds_read_b128 v[184:187], v142 offset:2048
	ds_read_b128 v[188:191], v142 offset:3072
	ds_read_b128 v[192:195], v142 offset:4096
	ds_read_b128 v[196:199], v142 offset:5120
	ds_read_b128 v[200:203], v142 offset:6144
	ds_read_b128 v[204:207], v142 offset:7168
	s_nop 0
	global_load_lds_dwordx4 v130, s[36:37]
	v_mov_b32_e32 v130, v138
	s_mov_b32 m0, s97
	s_nop 0
	global_load_lds_dwordx4 v130, s[36:37]
	s_waitcnt vmcnt(8)
	s_waitcnt lgkmcnt(0)
	s_barrier
; #define PG8_STAGE(bufoff, gbase, voff) do { if constexpr (!(Sched::CRIP & 2)) _Pragma("unroll") for (int _i = 0; _i < 2; ++_i) { unsigned _o = (voff)[_i]; asm volatile("" : "+v"(_o)); \
;         __builtin_amdgcn_global_load_lds((const unsigned*)((const char*)(gbase) + _o), (LAS unsigned*)(lds + (bufoff) + ldsw + _i * 8192), 16, 0, 0); } } while (0)
; #define PG8_LDA(dst, b, h) do { if constexpr (!(Sched::CRIP & 4)) _Pragma("unroll") for (int m = 0; m < 4; ++m) dst[m] = PG8_CAT(*(const LAS i32x4*)(lds + PG8_SA(b, h) + aoff + m * 2048), *(const LAS i32x4*)(lds + PG8_SA(b, h) + aoff + m * 2048 + 1024)); } while (0)
; #define PG8_WAIT_V(n) asm volatile("s_waitcnt vmcnt(" #n ")" ::: "memory")
; #define PG8_WAIT_L(n) asm volatile("s_waitcnt lgkmcnt(" #n ")" ::: "memory")
; #define PG8_BAR __builtin_amdgcn_s_barrier()
; #define PG8_SCHED __builtin_amdgcn_sched_barrier(0)
; template <class Epi, class Sched>
; __device__ __forceinline__ void gemm_phase(LAS unsigned char* lds, const Sched& S, const Epi& E) {
;     ...
;             PG8_WAIT_V(8); PG8_WAIT_L(0); PG8_BAR; PG8_MMA(0, 0, At, B0); PG8_MMA(0, 1, At, B1); PG8_BAR2; PG8_SCHED;
;             if constexpr (Sched::GATHER) { if (last && has_next) {
;                 int tz = threadIdx.x; asm volatile("" : "+v"(tz));
; #pragma unroll
;                 for (int i = 0; i < 2; ++i) { int R, C; stage_rc(tz * 16 + i * 8192, R, C);
; #pragma unroll
;                     for (int h = 0; h < 2; ++h) vA[h][i] = (unsigned)(lidx[h * HALF + R] * RP + C * 2); } } }
;             PG8_LDA(At, 0, 1); PG8_STAGE(PG8_SB(0, 0), b2, voffB); PG8_STAGE(PG8_SB(0, 1), b2 + hstep, voffB); PG8_STAGE(PG8_SA(0, 0), a2, vA[0]);
;             PG8_WAIT_V(8); PG8_WAIT_L(0); PG8_BAR; PG8_MMA(1, 0, At, B0); PG8_MMA(1, 1, At, B1); PG8_BAR2; PG8_SCHED;
	s_setprio 1
	s_waitcnt lgkmcnt(0)
	v_mfma_f32_16x16x32_bf16 v[126:129], v[144:147], v[176:179], v[126:129]
	v_mfma_f32_16x16x32_bf16 v[122:125], v[152:155], v[176:179], v[122:125]
	v_mfma_f32_16x16x32_bf16 v[118:121], v[144:147], v[184:187], v[118:121]
	v_mfma_f32_16x16x32_bf16 v[114:117], v[152:155], v[184:187], v[114:117]
	v_mfma_f32_16x16x32_bf16 v[102:105], v[144:147], v[192:195], v[102:105]
	v_mfma_f32_16x16x32_bf16 v[98:101], v[152:155], v[192:195], v[98:101]
	v_mfma_f32_16x16x32_bf16 v[86:89], v[144:147], v[200:203], v[86:89]
	v_mfma_f32_16x16x32_bf16 v[82:85], v[152:155], v[200:203], v[82:85]
	v_mfma_f32_16x16x32_bf16 v[126:129], v[148:151], v[180:183], v[126:129]
	v_mfma_f32_16x16x32_bf16 v[122:125], v[156:159], v[180:183], v[122:125]
	v_mfma_f32_16x16x32_bf16 v[118:121], v[148:151], v[188:191], v[118:121]
	v_mfma_f32_16x16x32_bf16 v[114:117], v[156:159], v[188:191], v[114:117]
	v_mfma_f32_16x16x32_bf16 v[102:105], v[148:151], v[196:199], v[102:105]
	v_mfma_f32_16x16x32_bf16 v[98:101], v[156:159], v[196:199], v[98:101]
	v_mfma_f32_16x16x32_bf16 v[86:89], v[148:151], v[204:207], v[86:89]
	v_mfma_f32_16x16x32_bf16 v[82:85], v[156:159], v[204:207], v[82:85]
	s_setprio 0
	s_setprio 1
	v_mfma_f32_16x16x32_bf16 v[110:113], v[160:163], v[176:179], v[110:113]
	v_mfma_f32_16x16x32_bf16 v[106:109], v[168:171], v[176:179], v[106:109]
	v_mfma_f32_16x16x32_bf16 v[94:97], v[160:163], v[184:187], v[94:97]
	v_mfma_f32_16x16x32_bf16 v[90:93], v[168:171], v[184:187], v[90:93]
	v_mfma_f32_16x16x32_bf16 v[78:81], v[160:163], v[192:195], v[78:81]
	v_mfma_f32_16x16x32_bf16 v[74:77], v[168:171], v[192:195], v[74:77]
	v_mfma_f32_16x16x32_bf16 v[70:73], v[160:163], v[200:203], v[70:73]
	v_mfma_f32_16x16x32_bf16 v[66:69], v[168:171], v[200:203], v[66:69]
	v_mfma_f32_16x16x32_bf16 v[110:113], v[164:167], v[180:183], v[110:113]
	v_mfma_f32_16x16x32_bf16 v[106:109], v[172:175], v[180:183], v[106:109]
	v_mfma_f32_16x16x32_bf16 v[94:97], v[164:167], v[188:191], v[94:97]
	v_mfma_f32_16x16x32_bf16 v[90:93], v[172:175], v[188:191], v[90:93]
	v_mfma_f32_16x16x32_bf16 v[78:81], v[164:167], v[196:199], v[78:81]
	v_mfma_f32_16x16x32_bf16 v[74:77], v[172:175], v[196:199], v[74:77]
	v_mfma_f32_16x16x32_bf16 v[70:73], v[164:167], v[204:207], v[70:73]
	v_mfma_f32_16x16x32_bf16 v[66:69], v[172:175], v[204:207], v[66:69]
	s_setprio 0
	s_barrier
	v_mov_b32_e32 v130, v1
	s_mov_b32 m0, vcc_lo
	ds_read_b128 v[176:179], v142 offset:16384
	ds_read_b128 v[180:183], v142 offset:17408
	ds_read_b128 v[184:187], v142 offset:18432
	ds_read_b128 v[188:191], v142 offset:19456
	ds_read_b128 v[192:195], v142 offset:20480
	ds_read_b128 v[196:199], v142 offset:21504
	ds_read_b128 v[200:203], v142 offset:22528
	ds_read_b128 v[204:207], v142 offset:23552
	s_cselect_b32 s36, s48, s94
	global_load_lds_dwordx4 v130, s[54:55]
	v_mov_b32_e32 v130, v134
	s_mov_b32 m0, vcc_hi
	s_cselect_b32 s37, s49, s95
	global_load_lds_dwordx4 v130, s[54:55]
	s_add_u32 s54, s54, 0x80000
	v_mov_b32_e32 v130, v1
	s_addc_u32 s55, s55, 0
	s_add_i32 s92, s76, s47
	s_mov_b32 m0, s92
	s_nop 0
	global_load_lds_dwordx4 v130, s[54:55]
	v_mov_b32_e32 v130, v134
	s_add_i32 m0, s92, 0x2000
	s_nop 0
	global_load_lds_dwordx4 v130, s[54:55]
	v_mov_b32_e32 v130, v135
	s_mov_b32 m0, s50
	s_nop 0
	global_load_lds_dwordx4 v130, s[34:35]
	v_mov_b32_e32 v130, v136
	s_mov_b32 m0, s51
	s_nop 0
	global_load_lds_dwordx4 v130, s[34:35]
	s_waitcnt vmcnt(8)
	s_waitcnt lgkmcnt(0)
	s_barrier
	s_setprio 1
	s_waitcnt lgkmcnt(0)
	v_mfma_f32_16x16x32_bf16 v[62:65], v[144:147], v[176:179], v[62:65]
	v_mfma_f32_16x16x32_bf16 v[58:61], v[152:155], v[176:179], v[58:61]
	v_mfma_f32_16x16x32_bf16 v[54:57], v[144:147], v[184:187], v[54:57]
	v_mfma_f32_16x16x32_bf16 v[50:53], v[152:155], v[184:187], v[50:53]
	v_mfma_f32_16x16x32_bf16 v[38:41], v[144:147], v[192:195], v[38:41]
	v_mfma_f32_16x16x32_bf16 v[34:37], v[152:155], v[192:195], v[34:37]
	v_mfma_f32_16x16x32_bf16 v[22:25], v[144:147], v[200:203], v[22:25]
	v_mfma_f32_16x16x32_bf16 v[18:21], v[152:155], v[200:203], v[18:21]
	v_mfma_f32_16x16x32_bf16 v[62:65], v[148:151], v[180:183], v[62:65]
	v_mfma_f32_16x16x32_bf16 v[58:61], v[156:159], v[180:183], v[58:61]
	v_mfma_f32_16x16x32_bf16 v[54:57], v[148:151], v[188:191], v[54:57]
	v_mfma_f32_16x16x32_bf16 v[50:53], v[156:159], v[188:191], v[50:53]
	v_mfma_f32_16x16x32_bf16 v[38:41], v[148:151], v[196:199], v[38:41]
	v_mfma_f32_16x16x32_bf16 v[34:37], v[156:159], v[196:199], v[34:37]
	v_mfma_f32_16x16x32_bf16 v[22:25], v[148:151], v[204:207], v[22:25]
	v_mfma_f32_16x16x32_bf16 v[18:21], v[156:159], v[204:207], v[18:21]
	s_setprio 0
	s_setprio 1
	v_mfma_f32_16x16x32_bf16 v[46:49], v[160:163], v[176:179], v[46:49]
	v_mfma_f32_16x16x32_bf16 v[42:45], v[168:171], v[176:179], v[42:45]
	v_mfma_f32_16x16x32_bf16 v[30:33], v[160:163], v[184:187], v[30:33]
	v_mfma_f32_16x16x32_bf16 v[26:29], v[168:171], v[184:187], v[26:29]
	v_mfma_f32_16x16x32_bf16 v[14:17], v[160:163], v[192:195], v[14:17]
	v_mfma_f32_16x16x32_bf16 v[10:13], v[168:171], v[192:195], v[10:13]
	v_mfma_f32_16x16x32_bf16 v[6:9], v[160:163], v[200:203], v[6:9]
	v_mfma_f32_16x16x32_bf16 v[2:5], v[168:171], v[200:203], v[2:5]
	v_mfma_f32_16x16x32_bf16 v[46:49], v[164:167], v[180:183], v[46:49]
	v_mfma_f32_16x16x32_bf16 v[42:45], v[172:175], v[180:183], v[42:45]
	v_mfma_f32_16x16x32_bf16 v[30:33], v[164:167], v[188:191], v[30:33]
	v_mfma_f32_16x16x32_bf16 v[26:29], v[172:175], v[188:191], v[26:29]
	v_mfma_f32_16x16x32_bf16 v[14:17], v[164:167], v[196:199], v[14:17]
	v_mfma_f32_16x16x32_bf16 v[10:13], v[172:175], v[196:199], v[10:13]
	v_mfma_f32_16x16x32_bf16 v[6:9], v[164:167], v[204:207], v[6:9]
	v_mfma_f32_16x16x32_bf16 v[2:5], v[172:175], v[204:207], v[2:5]
	s_setprio 0
	s_barrier
; #define PG8_STAGE(bufoff, gbase, voff) do { if constexpr (!(Sched::CRIP & 2)) _Pragma("unroll") for (int _i = 0; _i < 2; ++_i) { unsigned _o = (voff)[_i]; asm volatile("" : "+v"(_o)); \
;         __builtin_amdgcn_global_load_lds((const unsigned*)((const char*)(gbase) + _o), (LAS unsigned*)(lds + (bufoff) + ldsw + _i * 8192), 16, 0, 0); } } while (0)
; #define PG8_LDA(dst, b, h) do { if constexpr (!(Sched::CRIP & 4)) _Pragma("unroll") for (int m = 0; m < 4; ++m) dst[m] = PG8_CAT(*(const LAS i32x4*)(lds + PG8_SA(b, h) + aoff + m * 2048), *(const LAS i32x4*)(lds + PG8_SA(b, h) + aoff + m * 2048 + 1024)); } while (0)
; #define PG8_LDB(dst, b, h) do { if constexpr (!(Sched::CRIP & 4)) _Pragma("unroll") for (int n = 0; n < 2; ++n) dst[n] = PG8_CAT(*(const LAS i32x4*)(lds + PG8_SB(b, h) + boff + n * 2048), *(const LAS i32x4*)(lds + PG8_SB(b, h) + boff + n * 2048 + 1024)); } while (0)
; #define PG8_WAIT_V(n) asm volatile("s_waitcnt vmcnt(" #n ")" ::: "memory")
; #define PG8_WAIT_L(n) asm volatile("s_waitcnt lgkmcnt(" #n ")" ::: "memory")
; #define PG8_BAR __builtin_amdgcn_s_barrier()
; #define PG8_SCHED __builtin_amdgcn_sched_barrier(0)
; template <class Epi, class Sched>
; __device__ __forceinline__ void gemm_phase(LAS unsigned char* lds, const Sched& S, const Epi& E) {
;     ...
;             PG8_LDB(B0, 1, 0); PG8_LDB(B1, 1, 1); PG8_SCHED; PG8_LDA(At, 1, 0); PG8_STAGE(PG8_SA(0, 1), a2, vA[1]);
;             PG8_WAIT_V(8); PG8_WAIT_L(0); PG8_BAR; PG8_MMA(0, 0, At, B0); PG8_MMA(0, 1, At, B1); PG8_BAR2; PG8_SCHED;
	s_add_i32 s54, 0, 0x18000
	v_add_u32_e32 v130, s54, v139
	s_add_i32 s55, 0, 0x1c000
	ds_read_b128 v[144:147], v130
	ds_read_b128 v[148:151], v130 offset:1024
	ds_read_b128 v[152:155], v130 offset:2048
	ds_read_b128 v[156:159], v130 offset:3072
	v_add_u32_e32 v130, s55, v139
	ds_read_b128 v[160:163], v130
	ds_read_b128 v[164:167], v130 offset:1024
	ds_read_b128 v[168:171], v130 offset:2048
	ds_read_b128 v[172:175], v130 offset:3072
	v_mov_b32_e32 v130, v137
	s_mov_b32 m0, s66
	ds_read_b128 v[176:179], v142 offset:32768
	ds_read_b128 v[180:183], v142 offset:33792
	ds_read_b128 v[184:187], v142 offset:34816
	ds_read_b128 v[188:191], v142 offset:35840
	ds_read_b128 v[192:195], v142 offset:36864
	ds_read_b128 v[196:199], v142 offset:37888
	ds_read_b128 v[200:203], v142 offset:38912
	ds_read_b128 v[204:207], v142 offset:39936
	s_nop 0
	global_load_lds_dwordx4 v130, s[34:35]
	v_mov_b32_e32 v130, v138
	s_mov_b32 m0, s67
	s_nop 0
	global_load_lds_dwordx4 v130, s[34:35]
	s_waitcnt vmcnt(8)
	s_waitcnt lgkmcnt(0)
	s_barrier
	s_setprio 1
	s_waitcnt lgkmcnt(0)
	v_mfma_f32_16x16x32_bf16 v[126:129], v[144:147], v[176:179], v[126:129]
	v_mfma_f32_16x16x32_bf16 v[122:125], v[152:155], v[176:179], v[122:125]
	v_mfma_f32_16x16x32_bf16 v[118:121], v[144:147], v[184:187], v[118:121]
	v_mfma_f32_16x16x32_bf16 v[114:117], v[152:155], v[184:187], v[114:117]
	v_mfma_f32_16x16x32_bf16 v[102:105], v[144:147], v[192:195], v[102:105]
	v_mfma_f32_16x16x32_bf16 v[98:101], v[152:155], v[192:195], v[98:101]
	v_mfma_f32_16x16x32_bf16 v[86:89], v[144:147], v[200:203], v[86:89]
	v_mfma_f32_16x16x32_bf16 v[82:85], v[152:155], v[200:203], v[82:85]
	v_mfma_f32_16x16x32_bf16 v[126:129], v[148:151], v[180:183], v[126:129]
	v_mfma_f32_16x16x32_bf16 v[122:125], v[156:159], v[180:183], v[122:125]
	v_mfma_f32_16x16x32_bf16 v[118:121], v[148:151], v[188:191], v[118:121]
	v_mfma_f32_16x16x32_bf16 v[114:117], v[156:159], v[188:191], v[114:117]
	v_mfma_f32_16x16x32_bf16 v[102:105], v[148:151], v[196:199], v[102:105]
	v_mfma_f32_16x16x32_bf16 v[98:101], v[156:159], v[196:199], v[98:101]
	v_mfma_f32_16x16x32_bf16 v[86:89], v[148:151], v[204:207], v[86:89]
	v_mfma_f32_16x16x32_bf16 v[82:85], v[156:159], v[204:207], v[82:85]
	s_setprio 0
	s_setprio 1
	v_mfma_f32_16x16x32_bf16 v[110:113], v[160:163], v[176:179], v[110:113]
	v_mfma_f32_16x16x32_bf16 v[106:109], v[168:171], v[176:179], v[106:109]
	v_mfma_f32_16x16x32_bf16 v[94:97], v[160:163], v[184:187], v[94:97]
	v_mfma_f32_16x16x32_bf16 v[90:93], v[168:171], v[184:187], v[90:93]
	v_mfma_f32_16x16x32_bf16 v[78:81], v[160:163], v[192:195], v[78:81]
	v_mfma_f32_16x16x32_bf16 v[74:77], v[168:171], v[192:195], v[74:77]
	v_mfma_f32_16x16x32_bf16 v[70:73], v[160:163], v[200:203], v[70:73]
	v_mfma_f32_16x16x32_bf16 v[66:69], v[168:171], v[200:203], v[66:69]
	v_mfma_f32_16x16x32_bf16 v[110:113], v[164:167], v[180:183], v[110:113]
	v_mfma_f32_16x16x32_bf16 v[106:109], v[172:175], v[180:183], v[106:109]
	v_mfma_f32_16x16x32_bf16 v[94:97], v[164:167], v[188:191], v[94:97]
	v_mfma_f32_16x16x32_bf16 v[90:93], v[172:175], v[188:191], v[90:93]
	v_mfma_f32_16x16x32_bf16 v[78:81], v[164:167], v[196:199], v[78:81]
	v_mfma_f32_16x16x32_bf16 v[74:77], v[172:175], v[196:199], v[74:77]
	v_mfma_f32_16x16x32_bf16 v[70:73], v[164:167], v[204:207], v[70:73]
	v_mfma_f32_16x16x32_bf16 v[66:69], v[172:175], v[204:207], v[66:69]
	s_setprio 0
	s_barrier
; #define PG8_STAGE(bufoff, gbase, voff) do { if constexpr (!(Sched::CRIP & 2)) _Pragma("unroll") for (int _i = 0; _i < 2; ++_i) { unsigned _o = (voff)[_i]; asm volatile("" : "+v"(_o)); \
;         __builtin_amdgcn_global_load_lds((const unsigned*)((const char*)(gbase) + _o), (LAS unsigned*)(lds + (bufoff) + ldsw + _i * 8192), 16, 0, 0); } } while (0)
; #define PG8_LDA(dst, b, h) do { if constexpr (!(Sched::CRIP & 4)) _Pragma("unroll") for (int m = 0; m < 4; ++m) dst[m] = PG8_CAT(*(const LAS i32x4*)(lds + PG8_SA(b, h) + aoff + m * 2048), *(const LAS i32x4*)(lds + PG8_SA(b, h) + aoff + m * 2048 + 1024)); } while (0)
; #define PG8_WAIT_V(n) asm volatile("s_waitcnt vmcnt(" #n ")" ::: "memory")
; #define PG8_WAIT_L(n) asm volatile("s_waitcnt lgkmcnt(" #n ")" ::: "memory")
; #define PG8_BAR __builtin_amdgcn_s_barrier()
; #define PG8_SCHED __builtin_amdgcn_sched_barrier(0)
; template <class Epi, class Sched>
; __device__ __forceinline__ void gemm_phase(LAS unsigned char* lds, const Sched& S, const Epi& E) {
;     ...
;             PG8_LDA(At, 1, 1); PG8_STAGE(PG8_SB(1, 0), b3, voffB); PG8_STAGE(PG8_SB(1, 1), b3 + hstep, voffB); PG8_STAGE(PG8_SA(1, 0), a3, vA[0]);
;             PG8_WAIT_V(8); PG8_WAIT_L(0); PG8_BAR; PG8_MMA(1, 0, At, B0); PG8_MMA(1, 1, At, B1); PG8_BAR2; PG8_SCHED;
;             if constexpr (Sched::GATHER) { if (t == 0 && has_next && tid < 256) lidx[tid] = (tid < nxt.avalid) ? gi : 0; }
;         }
;         if constexpr (F8) asm volatile("s_nop 15\n\ts_nop 15" ::: "memory");
;         if (wr == 0) PG8_BAR;
;     __device__ __forceinline__ bool next(int i, Unit& u) const {
;         const int t = __builtin_amdgcn_readfirstlane(tk[i & 1]);
;         if (i > 0 && threadIdx.x == 0) tk[(i + 1) & 1] = (int)__hip_atomic_fetch_add(tick, 1u, __ATOMIC_RELAXED, __HIP_MEMORY_SCOPE_AGENT);
	v_mov_b32_e32 v130, v1
	s_add_i32 s34, s54, s47
	ds_read_b128 v[176:179], v142 offset:49152
	ds_read_b128 v[180:183], v142 offset:50176
	ds_read_b128 v[184:187], v142 offset:51200
	ds_read_b128 v[188:191], v142 offset:52224
	ds_read_b128 v[192:195], v142 offset:53248
	ds_read_b128 v[196:199], v142 offset:54272
	ds_read_b128 v[200:203], v142 offset:55296
	ds_read_b128 v[204:207], v142 offset:56320
	s_mov_b32 m0, s34
	s_nop 0
	global_load_lds_dwordx4 v130, s[36:37]
	v_mov_b32_e32 v130, v134
	s_add_i32 m0, s34, 0x2000
	s_add_u32 s34, s36, 0x80000
	global_load_lds_dwordx4 v130, s[36:37]
	s_addc_u32 s35, s37, 0
	v_mov_b32_e32 v130, v1
	s_add_i32 s36, s55, s47
	s_mov_b32 m0, s36
	s_nop 0
	global_load_lds_dwordx4 v130, s[34:35]
	v_mov_b32_e32 v130, v134
	s_add_i32 m0, s36, 0x2000
	s_nop 0
	global_load_lds_dwordx4 v130, s[34:35]
	v_mov_b32_e32 v130, v135
	s_mov_b32 m0, s70
	s_nop 0
	global_load_lds_dwordx4 v130, s[30:31]
	v_mov_b32_e32 v130, v136
	s_mov_b32 m0, s71
	s_nop 0
	global_load_lds_dwordx4 v130, s[30:31]
	s_waitcnt vmcnt(8)
	s_waitcnt lgkmcnt(0)
	s_barrier
	s_setprio 1
	s_waitcnt lgkmcnt(0)
	v_mfma_f32_16x16x32_bf16 v[62:65], v[144:147], v[176:179], v[62:65]
	v_mfma_f32_16x16x32_bf16 v[58:61], v[152:155], v[176:179], v[58:61]
	v_mfma_f32_16x16x32_bf16 v[54:57], v[144:147], v[184:187], v[54:57]
	v_mfma_f32_16x16x32_bf16 v[50:53], v[152:155], v[184:187], v[50:53]
	v_mfma_f32_16x16x32_bf16 v[38:41], v[144:147], v[192:195], v[38:41]
	v_mfma_f32_16x16x32_bf16 v[34:37], v[152:155], v[192:195], v[34:37]
	v_mfma_f32_16x16x32_bf16 v[22:25], v[144:147], v[200:203], v[22:25]
	v_mfma_f32_16x16x32_bf16 v[18:21], v[152:155], v[200:203], v[18:21]
	v_mfma_f32_16x16x32_bf16 v[62:65], v[148:151], v[180:183], v[62:65]
	v_mfma_f32_16x16x32_bf16 v[58:61], v[156:159], v[180:183], v[58:61]
	v_mfma_f32_16x16x32_bf16 v[54:57], v[148:151], v[188:191], v[54:57]
	v_mfma_f32_16x16x32_bf16 v[50:53], v[156:159], v[188:191], v[50:53]
	v_mfma_f32_16x16x32_bf16 v[38:41], v[148:151], v[196:199], v[38:41]
	v_mfma_f32_16x16x32_bf16 v[34:37], v[156:159], v[196:199], v[34:37]
	v_mfma_f32_16x16x32_bf16 v[22:25], v[148:151], v[204:207], v[22:25]
	v_mfma_f32_16x16x32_bf16 v[18:21], v[156:159], v[204:207], v[18:21]
	s_setprio 0
	s_setprio 1
	v_mfma_f32_16x16x32_bf16 v[46:49], v[160:163], v[176:179], v[46:49]
	v_mfma_f32_16x16x32_bf16 v[42:45], v[168:171], v[176:179], v[42:45]
	v_mfma_f32_16x16x32_bf16 v[30:33], v[160:163], v[184:187], v[30:33]
	v_mfma_f32_16x16x32_bf16 v[26:29], v[168:171], v[184:187], v[26:29]
	v_mfma_f32_16x16x32_bf16 v[14:17], v[160:163], v[192:195], v[14:17]
	v_mfma_f32_16x16x32_bf16 v[10:13], v[168:171], v[192:195], v[10:13]
	v_mfma_f32_16x16x32_bf16 v[6:9], v[160:163], v[200:203], v[6:9]
	v_mfma_f32_16x16x32_bf16 v[2:5], v[168:171], v[200:203], v[2:5]
	v_mfma_f32_16x16x32_bf16 v[46:49], v[164:167], v[180:183], v[46:49]
	v_mfma_f32_16x16x32_bf16 v[42:45], v[172:175], v[180:183], v[42:45]
	v_mfma_f32_16x16x32_bf16 v[30:33], v[164:167], v[188:191], v[30:33]
	v_mfma_f32_16x16x32_bf16 v[26:29], v[172:175], v[188:191], v[26:29]
	v_mfma_f32_16x16x32_bf16 v[14:17], v[164:167], v[196:199], v[14:17]
	v_mfma_f32_16x16x32_bf16 v[10:13], v[172:175], v[196:199], v[10:13]
	v_mfma_f32_16x16x32_bf16 v[6:9], v[164:167], v[204:207], v[6:9]
	v_mfma_f32_16x16x32_bf16 v[2:5], v[172:175], v[204:207], v[2:5]
	s_setprio 0
	s_barrier
	s_add_i32 s53, s53, 2
	s_addk_i32 s52, 0x100
	s_cmp_gt_u32 s53, 29
	s_cbranch_scc0 .LBB0_211
	s_and_saveexec_b64 s[98:99], s[0:1]
	s_cbranch_execz .Ltk_done
	s_and_b32 s100, s74, 1
	s_xor_b32 s100, s100, 1
	s_lshl_b32 s100, s100, 2
	s_add_i32 s100, s100, 0x27f00
	s_waitcnt vmcnt(8)
	v_readfirstlane_b32 s101, v246
	v_mov_b32_e32 v248, s100
	s_nop 0
	v_add_u32_e32 v247, s101, v247
	ds_write_b32 v248, v247
	s_waitcnt lgkmcnt(0)
.Ltk_done:
	s_or_b64 exec, exec, s[98:99]
	s_and_b64 vcc, exec, s[14:15]
	s_cbranch_vccz .LBB0_214
	s_barrier

; #define PG8_STAGE(bufoff, gbase, voff) do { if constexpr (!(Sched::CRIP & 2)) _Pragma("unroll") for (int _i = 0; _i < 2; ++_i) { unsigned _o = (voff)[_i]; asm volatile("" : "+v"(_o)); \
;         __builtin_amdgcn_global_load_lds((const unsigned*)((const char*)(gbase) + _o), (LAS unsigned*)(lds + (bufoff) + ldsw + _i * 8192), 16, 0, 0); } } while (0)
; #define PG8_WAIT_V(n) asm volatile("s_waitcnt vmcnt(" #n ")" ::: "memory")
; #define PG8_BAR __builtin_amdgcn_s_barrier()
; template <class Epi, class Sched>
; __device__ __forceinline__ void gemm_phase(LAS unsigned char* lds, const Sched& S, const Epi& E) {
;     ...
;     int crot = KROT(cur.pm, cur.pn);
;     PG8_STAGE(PG8_SB(0, 0), cB + PG8_KT(crot, 0), voffB); PG8_STAGE(PG8_SB(0, 1), cB + hstep + PG8_KT(crot, 0), voffB); PG8_STAGE(PG8_SA(0, 0), cA + PG8_KT(crot, 0), vA[0]); PG8_STAGE(PG8_SA(0, 1), cA + PG8_KT(crot, 0), vA[1]);
;     if (wr == 1) PG8_BAR;
;     PG8_WAIT_V(2); PG8_BAR;
;     PG8_STAGE(PG8_SB(1, 0), cB + PG8_KT(crot, 1), voffB); PG8_STAGE(PG8_SA(1, 0), cA + PG8_KT(crot, 1), vA[0]); PG8_STAGE(PG8_SB(1, 1), cB + hstep + PG8_KT(crot, 1), voffB);
;     PG8_WAIT_V(6); PG8_BAR;
.LBB0_562:
	s_add_u32 s10, s88, 0x5d800000
	s_addc_u32 s11, s89, 0
	s_add_u32 s12, s88, 0x6dc00000
	s_addc_u32 s13, s89, 0
	s_lshl_b32 s0, s0, 12
	s_and_b32 s21, s0, 0x3000
	s_lshl_b32 s0, s16, 7
	s_addk_i32 s0, 0x80
	s_lshl_b32 s20, s18, 13
	s_and_b32 s0, s0, 0x780
	s_add_u32 s18, s28, s0
	v_mov_b32_e32 v2, v1
	s_waitcnt vmcnt(2)
	s_barrier
	s_addc_u32 s19, s29, 0
	s_add_i32 m0, s50, 0x18000
	v_lshlrev_b32_e32 v3, 6, v0
	global_load_lds_dwordx4 v2, s[18:19]
	v_mov_b32_e32 v2, v194
	s_add_i32 m0, s50, 0x1a000
	v_lshlrev_b32_e32 v5, 2, v0
	global_load_lds_dwordx4 v2, s[18:19]
	s_add_u32 s18, s26, s0
	s_addc_u32 s19, s27, 0
	v_mov_b32_e32 v2, v195
	s_add_i32 s58, s50, 0x8000
	s_mov_b32 m0, s58
	s_add_i32 s59, s50, 0xa000
	global_load_lds_dwordx4 v2, s[18:19]
	v_mov_b32_e32 v2, v196
	s_mov_b32 m0, s59
	s_add_u32 s0, s1, s0
	global_load_lds_dwordx4 v2, s[18:19]
	v_mov_b32_e32 v2, v1
	s_addc_u32 s1, s15, 0
	s_add_i32 m0, s50, 0x1c000
	v_and_b32_e32 v3, 0x3c0, v3
	global_load_lds_dwordx4 v2, s[0:1]
	v_mov_b32_e32 v2, v194
	s_add_i32 m0, s50, 0x1e000
	v_and_b32_e32 v5, 32, v5
	global_load_lds_dwordx4 v2, s[0:1]
	v_and_b32_e32 v2, 48, v0
	v_or_b32_e32 v4, v3, v2
	v_bitop3_b32 v2, v3, v5, v2 bitop3:0x36
	s_waitcnt vmcnt(0)
	s_cmpk_lt_u32 s14, 0x100
	v_bitop3_b32 v3, s20, v4, v5 bitop3:0xf6
	v_or_b32_e32 v200, s21, v2
	s_cselect_b64 s[14:15], -1, 0
	s_add_i32 s62, 0, 0x10000
	s_add_i32 s63, 0, 0x14000
	v_mbcnt_lo_u32_b32 v2, -1, 0
	s_ashr_i32 s60, s96, 31
	s_ashr_i32 s61, s77, 31
	v_mov_b64_e32 v[178:179], 0x400
	v_mov_b64_e32 v[180:181], 0x3ff
	v_add_u32_e32 v201, s62, v200
	v_add_u32_e32 v202, s63, v200
	v_add_u32_e32 v203, 0, v3
	v_mbcnt_hi_u32_b32 v204, -1, v2
	s_mov_b32 s16, 0x39800000
	s_mov_b32 s64, 0
	s_mov_b64 s[22:23], s[26:27]
	s_mov_b64 s[24:25], s[28:29]
	s_barrier
	s_branch .LBB0_565

; #define PG8_STAGE(bufoff, gbase, voff) do { if constexpr (!(Sched::CRIP & 2)) _Pragma("unroll") for (int _i = 0; _i < 2; ++_i) { unsigned _o = (voff)[_i]; asm volatile("" : "+v"(_o)); \
;         __builtin_amdgcn_global_load_lds((const unsigned*)((const char*)(gbase) + _o), (LAS unsigned*)(lds + (bufoff) + ldsw + _i * 8192), 16, 0, 0); } } while (0)
; #define PG8_LDA(dst, b, h) do { if constexpr (!(Sched::CRIP & 4)) _Pragma("unroll") for (int m = 0; m < 4; ++m) dst[m] = PG8_CAT(*(const LAS i32x4*)(lds + PG8_SA(b, h) + aoff + m * 2048), *(const LAS i32x4*)(lds + PG8_SA(b, h) + aoff + m * 2048 + 1024)); } while (0)
; #define PG8_LDB(dst, b, h) do { if constexpr (!(Sched::CRIP & 4)) _Pragma("unroll") for (int n = 0; n < 2; ++n) dst[n] = PG8_CAT(*(const LAS i32x4*)(lds + PG8_SB(b, h) + boff + n * 2048), *(const LAS i32x4*)(lds + PG8_SB(b, h) + boff + n * 2048 + 1024)); } while (0)
; #define PG8_WAIT_V(n) asm volatile("s_waitcnt vmcnt(" #n ")" ::: "memory")
; #define PG8_WAIT_L(n) asm volatile("s_waitcnt lgkmcnt(" #n ")" ::: "memory")
; #define PG8_BAR __builtin_amdgcn_s_barrier()
; #define PG8_SCHED __builtin_amdgcn_sched_barrier(0)
; template <class Epi, class Sched>
; __device__ __forceinline__ void gemm_phase(LAS unsigned char* lds, const Sched& S, const Epi& E) {
;     ...
;             PG8_LDB(B0, 0, 0); PG8_LDB(B1, 0, 1); PG8_SCHED; PG8_LDA(At, 0, 0); PG8_STAGE(PG8_SA(1, 1), a1, vA[1]);
;             PG8_WAIT_V(8); PG8_WAIT_L(0); PG8_BAR; PG8_MMA(0, 0, At, B0); PG8_MMA(0, 1, At, B1); PG8_BAR2; PG8_SCHED;
;             if constexpr (Sched::GATHER) { if (last && has_next) {
;                 int tz = threadIdx.x; asm volatile("" : "+v"(tz));
; #pragma unroll
;                 for (int i = 0; i < 2; ++i) { int R, C; stage_rc(tz * 16 + i * 8192, R, C);
; #pragma unroll
;                     for (int h = 0; h < 2; ++h) vA[h][i] = (unsigned)(lidx[h * HALF + R] * RP + C * 2); } } }
;             PG8_LDA(At, 0, 1); PG8_STAGE(PG8_SB(0, 0), b2, voffB); PG8_STAGE(PG8_SB(0, 1), b2 + hstep, voffB); PG8_STAGE(PG8_SA(0, 0), a2, vA[0]);
;             PG8_WAIT_V(8); PG8_WAIT_L(0); PG8_BAR; PG8_MMA(1, 0, At, B0); PG8_MMA(1, 1, At, B1); PG8_BAR2; PG8_SCHED;
.LBB0_571:
	s_add_i32 s19, s20, s18
	s_and_b32 s19, s19, 15
	s_and_b64 s[30:31], s[0:1], exec
	s_cselect_b32 s21, s19, s34
	s_lshl_b32 s30, s21, 7
	s_add_u32 s21, s22, s30
	s_addc_u32 s39, s23, 0
	s_add_u32 s65, s24, s30
	s_addc_u32 s66, s25, 0
	s_addk_i32 s30, 0x80
	s_and_b32 s30, s30, 0x780
	s_add_u32 s67, s22, s30
	s_addc_u32 s70, s23, 0
	s_add_u32 s71, s24, s30
	s_addc_u32 s74, s25, 0
	s_lshl_b32 s30, s34, 7
	s_add_i32 s75, s30, 0x180
	s_mov_b32 s76, -2
	s_add_i32 s30, s75, 0xffffff00
	s_add_i32 s31, s75, 0xffffff80
	s_and_b32 s30, s30, 0x780
	s_and_b32 s31, s31, 0x780
	s_add_u32 s34, s26, s31
	s_addc_u32 s35, s27, 0
	s_add_u32 s41, s28, s31
	s_addc_u32 s42, s29, 0
	s_and_b32 s31, s75, 0x780
	s_add_u32 s43, s26, s31
	s_addc_u32 s48, s27, 0
	ds_read_b128 v[10:13], v201
	ds_read_b128 v[14:17], v201 offset:1024
	ds_read_b128 v[26:29], v201 offset:2048
	ds_read_b128 v[30:33], v201 offset:3072
	s_waitcnt lgkmcnt(0)
	ds_read_b128 v[2:5], v202
	ds_read_b128 v[6:9], v202 offset:1024
	ds_read_b128 v[18:21], v202 offset:2048
	ds_read_b128 v[22:25], v202 offset:3072
	s_add_u32 s36, s28, s31
	s_addc_u32 s37, s29, 0
	s_add_u32 s44, s26, s30
	s_addc_u32 s45, s27, 0
	s_add_i32 s52, s62, s47
	s_add_i32 m0, s50, 0xc000
	s_add_i32 s49, s50, 0xe000
	s_add_i32 s40, s52, 0x2000
	s_cmp_eq_u32 s76, 12
	s_cselect_b32 s35, s39, s35
	s_cselect_b32 s34, s21, s34
	s_cselect_b32 s31, s70, s48
	s_cselect_b32 s30, s67, s43
	s_cselect_b32 s43, s66, s42
	s_cselect_b32 s42, s65, s41
	v_mov_b32_e32 v190, v197
	ds_read_b128 v[162:165], v203
	ds_read_b128 v[166:169], v203 offset:1024
	ds_read_b128 v[170:173], v203 offset:2048
	ds_read_b128 v[174:177], v203 offset:3072
	ds_read_b128 v[182:185], v203 offset:4096
	ds_read_b128 v[186:189], v203 offset:5120
	ds_read_b128 v[214:217], v203 offset:6144
	ds_read_b128 v[218:221], v203 offset:7168
	s_nop 0
	global_load_lds_dwordx4 v190, s[44:45]
	v_mov_b32_e32 v190, v198
	s_mov_b32 m0, s49
	s_nop 0
	global_load_lds_dwordx4 v190, s[44:45]
	s_waitcnt vmcnt(63)
	s_waitcnt lgkmcnt(0)
	s_barrier
	s_setprio 1
	s_waitcnt lgkmcnt(0)
	s_nop 1
	v_mfma_scale_f32_16x16x128_f8f6f4 v[158:161], v[10:17], v[162:169], 0, v199, v199 op_sel_hi:[0,0,0]
	v_mfma_scale_f32_16x16x128_f8f6f4 v[154:157], v[26:33], v[162:169], 0, v199, v199 op_sel_hi:[0,0,0]
	v_mfma_scale_f32_16x16x128_f8f6f4 v[142:145], v[10:17], v[170:177], 0, v199, v199 op_sel_hi:[0,0,0]
	v_mfma_scale_f32_16x16x128_f8f6f4 v[138:141], v[26:33], v[170:177], 0, v199, v199 op_sel_hi:[0,0,0]
	v_mfma_scale_f32_16x16x128_f8f6f4 v[126:129], v[10:17], v[182:189], 0, v199, v199 op_sel_hi:[0,0,0]
	v_mfma_scale_f32_16x16x128_f8f6f4 v[122:125], v[26:33], v[182:189], 0, v199, v199 op_sel_hi:[0,0,0]
	v_mfma_scale_f32_16x16x128_f8f6f4 v[110:113], v[10:17], v[214:221], 0, v199, v199 op_sel_hi:[0,0,0]
	v_mfma_scale_f32_16x16x128_f8f6f4 v[106:109], v[26:33], v[214:221], 0, v199, v199 op_sel_hi:[0,0,0]
	s_setprio 0
	s_setprio 1
	s_nop 1
	v_mfma_scale_f32_16x16x128_f8f6f4 v[150:153], v[2:9], v[162:169], 0, v199, v199 op_sel_hi:[0,0,0]
	v_mfma_scale_f32_16x16x128_f8f6f4 v[146:149], v[18:25], v[162:169], 0, v199, v199 op_sel_hi:[0,0,0]
	v_mfma_scale_f32_16x16x128_f8f6f4 v[134:137], v[2:9], v[170:177], 0, v199, v199 op_sel_hi:[0,0,0]
	v_mfma_scale_f32_16x16x128_f8f6f4 v[130:133], v[18:25], v[170:177], 0, v199, v199 op_sel_hi:[0,0,0]
	v_mfma_scale_f32_16x16x128_f8f6f4 v[118:121], v[2:9], v[182:189], 0, v199, v199 op_sel_hi:[0,0,0]
	v_mfma_scale_f32_16x16x128_f8f6f4 v[114:117], v[18:25], v[182:189], 0, v199, v199 op_sel_hi:[0,0,0]
	v_mfma_scale_f32_16x16x128_f8f6f4 v[102:105], v[2:9], v[214:221], 0, v199, v199 op_sel_hi:[0,0,0]
	v_mfma_scale_f32_16x16x128_f8f6f4 v[98:101], v[18:25], v[214:221], 0, v199, v199 op_sel_hi:[0,0,0]
	s_setprio 0
	s_barrier
	v_mov_b32_e32 v190, v1
	s_mov_b32 m0, s52
	ds_read_b128 v[162:165], v203 offset:16384
	ds_read_b128 v[166:169], v203 offset:17408
	ds_read_b128 v[170:173], v203 offset:18432
	ds_read_b128 v[174:177], v203 offset:19456
	ds_read_b128 v[182:185], v203 offset:20480
	ds_read_b128 v[186:189], v203 offset:21504
	ds_read_b128 v[214:217], v203 offset:22528
	ds_read_b128 v[218:221], v203 offset:23552
	s_cselect_b32 s36, s71, s36
	global_load_lds_dwordx4 v190, s[42:43]
	v_mov_b32_e32 v190, v194
	s_mov_b32 m0, s40
	s_cselect_b32 s37, s74, s37
	s_add_u32 s40, s42, 0x40000
	global_load_lds_dwordx4 v190, s[42:43]
	v_mov_b32_e32 v190, v1
	s_addc_u32 s41, s43, 0
	s_add_i32 s42, s63, s47
	s_mov_b32 m0, s42
	s_nop 0
	global_load_lds_dwordx4 v190, s[40:41]
	v_mov_b32_e32 v190, v194
	s_add_i32 m0, s42, 0x2000
	s_nop 0
	global_load_lds_dwordx4 v190, s[40:41]
	v_mov_b32_e32 v190, v195
	s_mov_b32 m0, s50
	s_nop 0
	global_load_lds_dwordx4 v190, s[34:35]
	v_mov_b32_e32 v190, v196
	s_mov_b32 m0, s51
	s_nop 0
	global_load_lds_dwordx4 v190, s[34:35]
	s_waitcnt vmcnt(63)
	s_waitcnt lgkmcnt(0)
	s_barrier
; #define PG8_STAGE(bufoff, gbase, voff) do { if constexpr (!(Sched::CRIP & 2)) _Pragma("unroll") for (int _i = 0; _i < 2; ++_i) { unsigned _o = (voff)[_i]; asm volatile("" : "+v"(_o)); \
;         __builtin_amdgcn_global_load_lds((const unsigned*)((const char*)(gbase) + _o), (LAS unsigned*)(lds + (bufoff) + ldsw + _i * 8192), 16, 0, 0); } } while (0)
; #define PG8_LDA(dst, b, h) do { if constexpr (!(Sched::CRIP & 4)) _Pragma("unroll") for (int m = 0; m < 4; ++m) dst[m] = PG8_CAT(*(const LAS i32x4*)(lds + PG8_SA(b, h) + aoff + m * 2048), *(const LAS i32x4*)(lds + PG8_SA(b, h) + aoff + m * 2048 + 1024)); } while (0)
; #define PG8_LDB(dst, b, h) do { if constexpr (!(Sched::CRIP & 4)) _Pragma("unroll") for (int n = 0; n < 2; ++n) dst[n] = PG8_CAT(*(const LAS i32x4*)(lds + PG8_SB(b, h) + boff + n * 2048), *(const LAS i32x4*)(lds + PG8_SB(b, h) + boff + n * 2048 + 1024)); } while (0)
; #define PG8_WAIT_V(n) asm volatile("s_waitcnt vmcnt(" #n ")" ::: "memory")
; #define PG8_WAIT_L(n) asm volatile("s_waitcnt lgkmcnt(" #n ")" ::: "memory")
; #define PG8_BAR __builtin_amdgcn_s_barrier()
; #define PG8_SCHED __builtin_amdgcn_sched_barrier(0)
; template <class Epi, class Sched>
; __device__ __forceinline__ void gemm_phase(LAS unsigned char* lds, const Sched& S, const Epi& E) {
;     ...
;             PG8_WAIT_V(8); PG8_WAIT_L(0); PG8_BAR; PG8_MMA(1, 0, At, B0); PG8_MMA(1, 1, At, B1); PG8_BAR2; PG8_SCHED;
;             PG8_LDB(B0, 1, 0); PG8_LDB(B1, 1, 1); PG8_SCHED; PG8_LDA(At, 1, 0); PG8_STAGE(PG8_SA(0, 1), a2, vA[1]);
;             PG8_WAIT_V(8); PG8_WAIT_L(0); PG8_BAR; PG8_MMA(0, 0, At, B0); PG8_MMA(0, 1, At, B1); PG8_BAR2; PG8_SCHED;
	s_setprio 1
	s_waitcnt lgkmcnt(0)
	s_nop 1
	v_mfma_scale_f32_16x16x128_f8f6f4 v[94:97], v[10:17], v[162:169], 0, v199, v199 op_sel_hi:[0,0,0]
	v_mfma_scale_f32_16x16x128_f8f6f4 v[90:93], v[26:33], v[162:169], 0, v199, v199 op_sel_hi:[0,0,0]
	v_mfma_scale_f32_16x16x128_f8f6f4 v[78:81], v[10:17], v[170:177], 0, v199, v199 op_sel_hi:[0,0,0]
	v_mfma_scale_f32_16x16x128_f8f6f4 v[74:77], v[26:33], v[170:177], 0, v199, v199 op_sel_hi:[0,0,0]
	v_mfma_scale_f32_16x16x128_f8f6f4 v[62:65], v[10:17], v[182:189], 0, v199, v199 op_sel_hi:[0,0,0]
	v_mfma_scale_f32_16x16x128_f8f6f4 v[58:61], v[26:33], v[182:189], 0, v199, v199 op_sel_hi:[0,0,0]
	v_mfma_scale_f32_16x16x128_f8f6f4 v[46:49], v[10:17], v[214:221], 0, v199, v199 op_sel_hi:[0,0,0]
	v_mfma_scale_f32_16x16x128_f8f6f4 v[42:45], v[26:33], v[214:221], 0, v199, v199 op_sel_hi:[0,0,0]
	s_setprio 0
	s_setprio 1
	s_nop 1
	v_mfma_scale_f32_16x16x128_f8f6f4 v[86:89], v[2:9], v[162:169], 0, v199, v199 op_sel_hi:[0,0,0]
	v_mfma_scale_f32_16x16x128_f8f6f4 v[82:85], v[18:25], v[162:169], 0, v199, v199 op_sel_hi:[0,0,0]
	v_mfma_scale_f32_16x16x128_f8f6f4 v[70:73], v[2:9], v[170:177], 0, v199, v199 op_sel_hi:[0,0,0]
	v_mfma_scale_f32_16x16x128_f8f6f4 v[66:69], v[18:25], v[170:177], 0, v199, v199 op_sel_hi:[0,0,0]
	v_mfma_scale_f32_16x16x128_f8f6f4 v[54:57], v[2:9], v[182:189], 0, v199, v199 op_sel_hi:[0,0,0]
	v_mfma_scale_f32_16x16x128_f8f6f4 v[50:53], v[18:25], v[182:189], 0, v199, v199 op_sel_hi:[0,0,0]
	v_mfma_scale_f32_16x16x128_f8f6f4 v[38:41], v[2:9], v[214:221], 0, v199, v199 op_sel_hi:[0,0,0]
	v_mfma_scale_f32_16x16x128_f8f6f4 v[34:37], v[18:25], v[214:221], 0, v199, v199 op_sel_hi:[0,0,0]
	s_setprio 0
	s_barrier
	s_add_i32 s40, 0, 0x18000
	s_add_i32 s41, 0, 0x1c000
	v_add_u32_e32 v14, s40, v200
	v_add_u32_e32 v30, s41, v200
	ds_read_b128 v[2:5], v14
	ds_read_b128 v[6:9], v14 offset:1024
	ds_read_b128 v[10:13], v14 offset:2048
	ds_read_b128 v[14:17], v14 offset:3072
	ds_read_b128 v[18:21], v30
	ds_read_b128 v[22:25], v30 offset:1024
	ds_read_b128 v[26:29], v30 offset:2048
	ds_read_b128 v[30:33], v30 offset:3072
	v_mov_b32_e32 v190, v197
	s_mov_b32 m0, s56
	ds_read_b128 v[162:165], v203 offset:32768
	ds_read_b128 v[166:169], v203 offset:33792
	ds_read_b128 v[170:173], v203 offset:34816
	ds_read_b128 v[174:177], v203 offset:35840
	ds_read_b128 v[182:185], v203 offset:36864
	ds_read_b128 v[186:189], v203 offset:37888
	ds_read_b128 v[214:217], v203 offset:38912
	ds_read_b128 v[218:221], v203 offset:39936
	s_nop 0
	global_load_lds_dwordx4 v190, s[34:35]
	v_mov_b32_e32 v190, v198
	s_mov_b32 m0, s57
	s_nop 0
	global_load_lds_dwordx4 v190, s[34:35]
	s_waitcnt vmcnt(8)
	s_waitcnt lgkmcnt(0)
	s_barrier
	s_setprio 1
	s_waitcnt lgkmcnt(0)
	s_nop 1
	v_mfma_scale_f32_16x16x128_f8f6f4 v[158:161], v[2:9], v[162:169], v[158:161], v199, v199 op_sel_hi:[0,0,0]
	v_mfma_scale_f32_16x16x128_f8f6f4 v[154:157], v[10:17], v[162:169], v[154:157], v199, v199 op_sel_hi:[0,0,0]
	v_mfma_scale_f32_16x16x128_f8f6f4 v[142:145], v[2:9], v[170:177], v[142:145], v199, v199 op_sel_hi:[0,0,0]
	v_mfma_scale_f32_16x16x128_f8f6f4 v[138:141], v[10:17], v[170:177], v[138:141], v199, v199 op_sel_hi:[0,0,0]
	v_mfma_scale_f32_16x16x128_f8f6f4 v[126:129], v[2:9], v[182:189], v[126:129], v199, v199 op_sel_hi:[0,0,0]
	v_mfma_scale_f32_16x16x128_f8f6f4 v[122:125], v[10:17], v[182:189], v[122:125], v199, v199 op_sel_hi:[0,0,0]
	v_mfma_scale_f32_16x16x128_f8f6f4 v[110:113], v[2:9], v[214:221], v[110:113], v199, v199 op_sel_hi:[0,0,0]
	v_mfma_scale_f32_16x16x128_f8f6f4 v[106:109], v[10:17], v[214:221], v[106:109], v199, v199 op_sel_hi:[0,0,0]
	s_setprio 0
	s_setprio 1
	s_nop 1
	v_mfma_scale_f32_16x16x128_f8f6f4 v[150:153], v[18:25], v[162:169], v[150:153], v199, v199 op_sel_hi:[0,0,0]
	v_mfma_scale_f32_16x16x128_f8f6f4 v[146:149], v[26:33], v[162:169], v[146:149], v199, v199 op_sel_hi:[0,0,0]
	v_mfma_scale_f32_16x16x128_f8f6f4 v[134:137], v[18:25], v[170:177], v[134:137], v199, v199 op_sel_hi:[0,0,0]
	v_mfma_scale_f32_16x16x128_f8f6f4 v[130:133], v[26:33], v[170:177], v[130:133], v199, v199 op_sel_hi:[0,0,0]
	v_mfma_scale_f32_16x16x128_f8f6f4 v[118:121], v[18:25], v[182:189], v[118:121], v199, v199 op_sel_hi:[0,0,0]
	v_mfma_scale_f32_16x16x128_f8f6f4 v[114:117], v[26:33], v[182:189], v[114:117], v199, v199 op_sel_hi:[0,0,0]
	v_mfma_scale_f32_16x16x128_f8f6f4 v[102:105], v[18:25], v[214:221], v[102:105], v199, v199 op_sel_hi:[0,0,0]
	v_mfma_scale_f32_16x16x128_f8f6f4 v[98:101], v[26:33], v[214:221], v[98:101], v199, v199 op_sel_hi:[0,0,0]
	s_setprio 0
	s_barrier
; #define PG8_STAGE(bufoff, gbase, voff) do { if constexpr (!(Sched::CRIP & 2)) _Pragma("unroll") for (int _i = 0; _i < 2; ++_i) { unsigned _o = (voff)[_i]; asm volatile("" : "+v"(_o)); \
;         __builtin_amdgcn_global_load_lds((const unsigned*)((const char*)(gbase) + _o), (LAS unsigned*)(lds + (bufoff) + ldsw + _i * 8192), 16, 0, 0); } } while (0)
; #define PG8_LDA(dst, b, h) do { if constexpr (!(Sched::CRIP & 4)) _Pragma("unroll") for (int m = 0; m < 4; ++m) dst[m] = PG8_CAT(*(const LAS i32x4*)(lds + PG8_SA(b, h) + aoff + m * 2048), *(const LAS i32x4*)(lds + PG8_SA(b, h) + aoff + m * 2048 + 1024)); } while (0)
; #define PG8_WAIT_V(n) asm volatile("s_waitcnt vmcnt(" #n ")" ::: "memory")
; #define PG8_WAIT_L(n) asm volatile("s_waitcnt lgkmcnt(" #n ")" ::: "memory")
; #define PG8_BAR __builtin_amdgcn_s_barrier()
; #define PG8_SCHED __builtin_amdgcn_sched_barrier(0)
; template <class Epi, class Sched>
; __device__ __forceinline__ void gemm_phase(LAS unsigned char* lds, const Sched& S, const Epi& E) {
;     ...
;             PG8_LDA(At, 1, 1); PG8_STAGE(PG8_SB(1, 0), b3, voffB); PG8_STAGE(PG8_SB(1, 1), b3 + hstep, voffB); PG8_STAGE(PG8_SA(1, 0), a3, vA[0]);
;             PG8_WAIT_V(8); PG8_WAIT_L(0); PG8_BAR; PG8_MMA(1, 0, At, B0); PG8_MMA(1, 1, At, B1); PG8_BAR2; PG8_SCHED;
	v_mov_b32_e32 v190, v1
	s_add_i32 s34, s40, s47
	ds_read_b128 v[162:165], v203 offset:49152
	ds_read_b128 v[166:169], v203 offset:50176
	ds_read_b128 v[170:173], v203 offset:51200
	ds_read_b128 v[174:177], v203 offset:52224
	ds_read_b128 v[182:185], v203 offset:53248
	ds_read_b128 v[186:189], v203 offset:54272
	ds_read_b128 v[214:217], v203 offset:55296
	ds_read_b128 v[218:221], v203 offset:56320
	s_mov_b32 m0, s34
	s_nop 0
	global_load_lds_dwordx4 v190, s[36:37]
	v_mov_b32_e32 v190, v194
	s_add_i32 m0, s34, 0x2000
	s_add_u32 s34, s36, 0x40000
	global_load_lds_dwordx4 v190, s[36:37]
	s_addc_u32 s35, s37, 0
	v_mov_b32_e32 v190, v1
	s_add_i32 s36, s41, s47
	s_mov_b32 m0, s36
	s_nop 0
	global_load_lds_dwordx4 v190, s[34:35]
	v_mov_b32_e32 v190, v194
	s_add_i32 m0, s36, 0x2000
	s_nop 0
	global_load_lds_dwordx4 v190, s[34:35]
	v_mov_b32_e32 v190, v195
	s_mov_b32 m0, s58
	s_nop 0
	global_load_lds_dwordx4 v190, s[30:31]
	v_mov_b32_e32 v190, v196
	s_mov_b32 m0, s59
	s_nop 0
	global_load_lds_dwordx4 v190, s[30:31]
	s_waitcnt vmcnt(8)
	s_waitcnt lgkmcnt(0)
	s_barrier
	s_setprio 1
	s_waitcnt lgkmcnt(0)
	s_nop 1
	v_mfma_scale_f32_16x16x128_f8f6f4 v[94:97], v[2:9], v[162:169], v[94:97], v199, v199 op_sel_hi:[0,0,0]
	v_mfma_scale_f32_16x16x128_f8f6f4 v[90:93], v[10:17], v[162:169], v[90:93], v199, v199 op_sel_hi:[0,0,0]
	v_mfma_scale_f32_16x16x128_f8f6f4 v[78:81], v[2:9], v[170:177], v[78:81], v199, v199 op_sel_hi:[0,0,0]
	v_mfma_scale_f32_16x16x128_f8f6f4 v[74:77], v[10:17], v[170:177], v[74:77], v199, v199 op_sel_hi:[0,0,0]
	v_mfma_scale_f32_16x16x128_f8f6f4 v[62:65], v[2:9], v[182:189], v[62:65], v199, v199 op_sel_hi:[0,0,0]
	v_mfma_scale_f32_16x16x128_f8f6f4 v[58:61], v[10:17], v[182:189], v[58:61], v199, v199 op_sel_hi:[0,0,0]
	v_mfma_scale_f32_16x16x128_f8f6f4 v[46:49], v[2:9], v[214:221], v[46:49], v199, v199 op_sel_hi:[0,0,0]
	v_mfma_scale_f32_16x16x128_f8f6f4 v[42:45], v[10:17], v[214:221], v[42:45], v199, v199 op_sel_hi:[0,0,0]
	s_setprio 0
	s_setprio 1
	s_nop 1
	v_mfma_scale_f32_16x16x128_f8f6f4 v[86:89], v[18:25], v[162:169], v[86:89], v199, v199 op_sel_hi:[0,0,0]
	v_mfma_scale_f32_16x16x128_f8f6f4 v[82:85], v[26:33], v[162:169], v[82:85], v199, v199 op_sel_hi:[0,0,0]
	v_mfma_scale_f32_16x16x128_f8f6f4 v[70:73], v[18:25], v[170:177], v[70:73], v199, v199 op_sel_hi:[0,0,0]
	v_mfma_scale_f32_16x16x128_f8f6f4 v[66:69], v[26:33], v[170:177], v[66:69], v199, v199 op_sel_hi:[0,0,0]
	v_mfma_scale_f32_16x16x128_f8f6f4 v[54:57], v[18:25], v[182:189], v[54:57], v199, v199 op_sel_hi:[0,0,0]
	v_mfma_scale_f32_16x16x128_f8f6f4 v[50:53], v[26:33], v[182:189], v[50:53], v199, v199 op_sel_hi:[0,0,0]
	v_mfma_scale_f32_16x16x128_f8f6f4 v[38:41], v[18:25], v[214:221], v[38:41], v199, v199 op_sel_hi:[0,0,0]
	v_mfma_scale_f32_16x16x128_f8f6f4 v[34:37], v[26:33], v[214:221], v[34:37], v199, v199 op_sel_hi:[0,0,0]
	s_setprio 0
	s_barrier
	s_add_i32 s76, s76, 2
	s_addk_i32 s75, 0x100

; #define PG8_STAGE(bufoff, gbase, voff) do { if constexpr (!(Sched::CRIP & 2)) _Pragma("unroll") for (int _i = 0; _i < 2; ++_i) { unsigned _o = (voff)[_i]; asm volatile("" : "+v"(_o)); \
;         __builtin_amdgcn_global_load_lds((const unsigned*)((const char*)(gbase) + _o), (LAS unsigned*)(lds + (bufoff) + ldsw + _i * 8192), 16, 0, 0); } } while (0)
; #define PG8_WAIT_V(n) asm volatile("s_waitcnt vmcnt(" #n ")" ::: "memory")
; #define PG8_BAR __builtin_amdgcn_s_barrier()
; template <class Epi, class Sched>
; __device__ __forceinline__ void gemm_phase(LAS unsigned char* lds, const Sched& S, const Epi& E) {
;     ...
;     int crot = KROT(cur.pm, cur.pn);
;     PG8_STAGE(PG8_SB(0, 0), cB + PG8_KT(crot, 0), voffB); PG8_STAGE(PG8_SB(0, 1), cB + hstep + PG8_KT(crot, 0), voffB); PG8_STAGE(PG8_SA(0, 0), cA + PG8_KT(crot, 0), vA[0]); PG8_STAGE(PG8_SA(0, 1), cA + PG8_KT(crot, 0), vA[1]);
;     if (wr == 1) PG8_BAR;
;     PG8_WAIT_V(2); PG8_BAR;
;     PG8_STAGE(PG8_SB(1, 0), cB + PG8_KT(crot, 1), voffB); PG8_STAGE(PG8_SA(1, 0), cA + PG8_KT(crot, 1), vA[0]); PG8_STAGE(PG8_SB(1, 1), cB + hstep + PG8_KT(crot, 1), voffB);
;     PG8_WAIT_V(6); PG8_BAR;
.LBB0_801:
	s_add_u32 s6, s88, 0x1000000
	s_addc_u32 s7, s89, 0
	s_lshl_b32 s14, s8, 13
	s_lshl_b32 s8, s24, 7
	s_lshl_b32 s1, s1, 12
	s_addk_i32 s8, 0x80
	s_and_b32 s1, s1, 0x3000
	s_and_b32 s8, s8, 0x780
	s_add_u32 s12, s28, s8
	v_mov_b32_e32 v2, v1
	s_waitcnt vmcnt(2)
	s_barrier
	s_addc_u32 s13, s29, 0
	s_add_i32 m0, s69, 0x18000
	v_lshlrev_b32_e32 v3, 6, v0
	global_load_lds_dwordx4 v2, s[12:13]
	v_mov_b32_e32 v2, v180
	s_add_i32 m0, s69, 0x1a000
	v_and_b32_e32 v3, 0x3c0, v3
	global_load_lds_dwordx4 v2, s[12:13]
	s_add_u32 s12, s26, s8
	s_addc_u32 s13, s27, 0
	v_mov_b32_e32 v2, v181
	s_add_i32 s74, s69, 0x8000
	s_mov_b32 m0, s74
	s_add_i32 s75, s69, 0xa000
	global_load_lds_dwordx4 v2, s[12:13]
	v_mov_b32_e32 v2, v182
	s_mov_b32 m0, s75
	s_add_u32 s8, s9, s8
	global_load_lds_dwordx4 v2, s[12:13]
	v_mov_b32_e32 v2, v1
	s_addc_u32 s9, s10, 0
	s_add_i32 m0, s69, 0x1c000
	v_lshlrev_b32_e32 v5, 2, v0
	global_load_lds_dwordx4 v2, s[8:9]
	v_mov_b32_e32 v2, v180
	s_add_i32 m0, s69, 0x1e000
	v_and_b32_e32 v5, 32, v5
	global_load_lds_dwordx4 v2, s[8:9]
	v_and_b32_e32 v2, 48, v0
	v_or_b32_e32 v4, v3, v2
	s_waitcnt vmcnt(0)
	s_cmpk_lt_u32 s0, 0x100
	v_bitop3_b32 v2, v3, v5, v2 bitop3:0x36
	v_bitop3_b32 v3, s14, v4, v5 bitop3:0xf6
	s_cselect_b64 s[8:9], -1, 0
	s_add_i32 s0, 0, 0x27d80
	v_or_b32_e32 v186, s1, v2
	s_ashr_i32 s76, s96, 31
	v_mov_b32_e32 v187, s0
	s_add_i32 s77, 0, 0x10000
	s_add_i32 s78, 0, 0x14000
	v_add_u32_e32 v188, 0, v3
	v_mov_b32_e32 v179, 0
	s_mov_b32 s10, 0x3a800000
	s_mov_b32 s79, 0xc3e00000
	v_mov_b32_e32 v189, 0x43e00000
	s_mov_b64 s[94:95], s[28:29]
	s_mov_b64 s[92:93], s[26:27]
	v_readlane_b32 s38, v255, 28
	s_barrier
	s_branch .LBB0_804

; #define PG8_STAGE(bufoff, gbase, voff) do { if constexpr (!(Sched::CRIP & 2)) _Pragma("unroll") for (int _i = 0; _i < 2; ++_i) { unsigned _o = (voff)[_i]; asm volatile("" : "+v"(_o)); \
;         __builtin_amdgcn_global_load_lds((const unsigned*)((const char*)(gbase) + _o), (LAS unsigned*)(lds + (bufoff) + ldsw + _i * 8192), 16, 0, 0); } } while (0)
; #define PG8_LDA(dst, b, h) do { if constexpr (!(Sched::CRIP & 4)) _Pragma("unroll") for (int m = 0; m < 4; ++m) dst[m] = PG8_CAT(*(const LAS i32x4*)(lds + PG8_SA(b, h) + aoff + m * 2048), *(const LAS i32x4*)(lds + PG8_SA(b, h) + aoff + m * 2048 + 1024)); } while (0)
; #define PG8_LDB(dst, b, h) do { if constexpr (!(Sched::CRIP & 4)) _Pragma("unroll") for (int n = 0; n < 2; ++n) dst[n] = PG8_CAT(*(const LAS i32x4*)(lds + PG8_SB(b, h) + boff + n * 2048), *(const LAS i32x4*)(lds + PG8_SB(b, h) + boff + n * 2048 + 1024)); } while (0)
; #define PG8_WAIT_V(n) asm volatile("s_waitcnt vmcnt(" #n ")" ::: "memory")
; #define PG8_WAIT_L(n) asm volatile("s_waitcnt lgkmcnt(" #n ")" ::: "memory")
; #define PG8_BAR __builtin_amdgcn_s_barrier()
; #define PG8_SCHED __builtin_amdgcn_sched_barrier(0)
; template <class Epi, class Sched>
; __device__ __forceinline__ void gemm_phase(LAS unsigned char* lds, const Sched& S, const Epi& E) {
;     ...
;             PG8_LDB(B0, 0, 0); PG8_LDB(B1, 0, 1); PG8_SCHED; PG8_LDA(At, 0, 0); PG8_STAGE(PG8_SA(1, 1), a1, vA[1]);
;             PG8_WAIT_V(8); PG8_WAIT_L(0); PG8_BAR; PG8_MMA(0, 0, At, B0); PG8_MMA(0, 1, At, B1); PG8_BAR2; PG8_SCHED;
;             if constexpr (Sched::GATHER) { if (last && has_next) {
;                 int tz = threadIdx.x; asm volatile("" : "+v"(tz));
; #pragma unroll
;                 for (int i = 0; i < 2; ++i) { int R, C; stage_rc(tz * 16 + i * 8192, R, C);
; #pragma unroll
;                     for (int h = 0; h < 2; ++h) vA[h][i] = (unsigned)(lidx[h * HALF + R] * RP + C * 2); } } }
;             PG8_LDA(At, 0, 1); PG8_STAGE(PG8_SB(0, 0), b2, voffB); PG8_STAGE(PG8_SB(0, 1), b2 + hstep, voffB); PG8_STAGE(PG8_SA(0, 0), a2, vA[0]);
;             PG8_WAIT_V(8); PG8_WAIT_L(0); PG8_BAR; PG8_MMA(1, 0, At, B0); PG8_MMA(1, 1, At, B1); PG8_BAR2; PG8_SCHED;
.LBB0_806:
	s_and_b32 s13, s12, 15
	s_and_b64 s[30:31], s[0:1], exec
	s_cselect_b32 s15, s13, s34
	s_lshl_b32 s30, s15, 7
	s_add_u32 s15, s92, s30
	s_addc_u32 s17, s93, 0
	s_add_u32 s25, s94, s30
	s_addc_u32 s38, s95, 0
	s_addk_i32 s30, 0x80
	s_and_b32 s30, s30, 0x780
	s_add_u32 s39, s92, s30
	s_addc_u32 s80, s93, 0
	s_add_u32 s81, s94, s30
	s_addc_u32 s82, s95, 0
	s_lshl_b32 s30, s34, 7
	s_add_i32 s83, s30, 0x180
	s_mov_b32 s84, -2
	s_add_i32 s30, s83, 0xffffff00
	s_add_i32 s31, s83, 0xffffff80
	s_and_b32 s30, s30, 0x780
	s_and_b32 s31, s31, 0x780
	s_add_u32 s34, s26, s31
	s_addc_u32 s35, s27, 0
	s_add_u32 s40, s28, s31
	s_addc_u32 s41, s29, 0
	s_and_b32 s31, s83, 0x780
	s_add_u32 s53, s26, s31
	v_add_u32_e32 v2, s77, v186
	v_add_u32_e32 v22, s78, v186
	s_addc_u32 s85, s27, 0
	ds_read_b128 v[10:13], v2
	ds_read_b128 v[14:17], v2 offset:1024
	ds_read_b128 v[26:29], v2 offset:2048
	ds_read_b128 v[30:33], v2 offset:3072
	ds_read_b128 v[2:5], v22
	ds_read_b128 v[6:9], v22 offset:1024
	ds_read_b128 v[18:21], v22 offset:2048
	ds_read_b128 v[22:25], v22 offset:3072
	s_add_u32 s36, s28, s31
	s_addc_u32 s37, s29, 0
	s_add_u32 s54, s26, s30
	s_addc_u32 s55, s27, 0
	s_add_i32 s87, s77, s47
	s_add_i32 m0, s69, 0xc000
	s_add_i32 s86, s69, 0xe000
	s_add_i32 s52, s87, 0x2000
	s_cmp_eq_u32 s84, 12
	s_cselect_b32 s35, s17, s35
	s_cselect_b32 s34, s15, s34
	s_cselect_b32 s31, s80, s85
	s_cselect_b32 s30, s39, s53
	s_cselect_b32 s41, s38, s41
	s_cselect_b32 s40, s25, s40
	v_mov_b32_e32 v178, v183
	ds_read_b128 v[198:201], v188
	ds_read_b128 v[202:205], v188 offset:1024
	ds_read_b128 v[214:217], v188 offset:2048
	ds_read_b128 v[218:221], v188 offset:3072
	ds_read_b128 v[222:225], v188 offset:4096
	ds_read_b128 v[226:229], v188 offset:5120
	ds_read_b128 v[230:233], v188 offset:6144
	ds_read_b128 v[234:237], v188 offset:7168
	s_nop 0
	global_load_lds_dwordx4 v178, s[54:55]
	v_mov_b32_e32 v178, v184
	s_mov_b32 m0, s86
	s_nop 0
	global_load_lds_dwordx4 v178, s[54:55]
	s_waitcnt vmcnt(28)
	s_waitcnt lgkmcnt(0)
	s_barrier
	s_setprio 1
	s_waitcnt lgkmcnt(0)
	s_nop 1
	v_mfma_scale_f32_16x16x128_f8f6f4 v[174:177], v[10:17], v[198:205], 0, v185, v185 op_sel_hi:[0,0,0]
	v_mfma_scale_f32_16x16x128_f8f6f4 v[170:173], v[26:33], v[198:205], 0, v185, v185 op_sel_hi:[0,0,0]
	v_mfma_scale_f32_16x16x128_f8f6f4 v[166:169], v[10:17], v[214:221], 0, v185, v185 op_sel_hi:[0,0,0]
	v_mfma_scale_f32_16x16x128_f8f6f4 v[162:165], v[26:33], v[214:221], 0, v185, v185 op_sel_hi:[0,0,0]
	v_mfma_scale_f32_16x16x128_f8f6f4 v[142:145], v[10:17], v[222:229], 0, v185, v185 op_sel_hi:[0,0,0]
	v_mfma_scale_f32_16x16x128_f8f6f4 v[138:141], v[26:33], v[222:229], 0, v185, v185 op_sel_hi:[0,0,0]
	v_mfma_scale_f32_16x16x128_f8f6f4 v[134:137], v[10:17], v[230:237], 0, v185, v185 op_sel_hi:[0,0,0]
	v_mfma_scale_f32_16x16x128_f8f6f4 v[130:133], v[26:33], v[230:237], 0, v185, v185 op_sel_hi:[0,0,0]
	s_setprio 0
	s_setprio 1
	s_nop 1
	v_mfma_scale_f32_16x16x128_f8f6f4 v[158:161], v[2:9], v[198:205], 0, v185, v185 op_sel_hi:[0,0,0]
	v_mfma_scale_f32_16x16x128_f8f6f4 v[154:157], v[18:25], v[198:205], 0, v185, v185 op_sel_hi:[0,0,0]
	v_mfma_scale_f32_16x16x128_f8f6f4 v[150:153], v[2:9], v[214:221], 0, v185, v185 op_sel_hi:[0,0,0]
	v_mfma_scale_f32_16x16x128_f8f6f4 v[146:149], v[18:25], v[214:221], 0, v185, v185 op_sel_hi:[0,0,0]
	v_mfma_scale_f32_16x16x128_f8f6f4 v[126:129], v[2:9], v[222:229], 0, v185, v185 op_sel_hi:[0,0,0]
	v_mfma_scale_f32_16x16x128_f8f6f4 v[122:125], v[18:25], v[222:229], 0, v185, v185 op_sel_hi:[0,0,0]
	v_mfma_scale_f32_16x16x128_f8f6f4 v[118:121], v[2:9], v[230:237], 0, v185, v185 op_sel_hi:[0,0,0]
	v_mfma_scale_f32_16x16x128_f8f6f4 v[114:117], v[18:25], v[230:237], 0, v185, v185 op_sel_hi:[0,0,0]
	s_setprio 0
	s_barrier
	v_mov_b32_e32 v178, v1
	s_mov_b32 m0, s87
	ds_read_b128 v[198:201], v188 offset:16384
	ds_read_b128 v[202:205], v188 offset:17408
	ds_read_b128 v[214:217], v188 offset:18432
	ds_read_b128 v[218:221], v188 offset:19456
	ds_read_b128 v[222:225], v188 offset:20480
	ds_read_b128 v[226:229], v188 offset:21504
	ds_read_b128 v[230:233], v188 offset:22528
	ds_read_b128 v[234:237], v188 offset:23552
	s_cselect_b32 s36, s81, s36
	global_load_lds_dwordx4 v178, s[40:41]
	v_mov_b32_e32 v178, v180
	s_mov_b32 m0, s52
	s_cselect_b32 s37, s82, s37
	global_load_lds_dwordx4 v178, s[40:41]
	s_add_u32 s40, s40, 0x40000
	v_mov_b32_e32 v178, v1
	s_addc_u32 s41, s41, 0
	s_add_i32 s52, s78, s47
	s_mov_b32 m0, s52
	s_nop 0
	global_load_lds_dwordx4 v178, s[40:41]
	v_mov_b32_e32 v178, v180
	s_add_i32 m0, s52, 0x2000
	s_nop 0
	global_load_lds_dwordx4 v178, s[40:41]
	v_mov_b32_e32 v178, v181
	s_mov_b32 m0, s69
	s_nop 0
	global_load_lds_dwordx4 v178, s[34:35]
	v_mov_b32_e32 v178, v182
	s_mov_b32 m0, s70
	s_nop 0
	global_load_lds_dwordx4 v178, s[34:35]
	s_waitcnt vmcnt(28)
	s_waitcnt lgkmcnt(0)
	s_barrier
; #define PG8_STAGE(bufoff, gbase, voff) do { if constexpr (!(Sched::CRIP & 2)) _Pragma("unroll") for (int _i = 0; _i < 2; ++_i) { unsigned _o = (voff)[_i]; asm volatile("" : "+v"(_o)); \
;         __builtin_amdgcn_global_load_lds((const unsigned*)((const char*)(gbase) + _o), (LAS unsigned*)(lds + (bufoff) + ldsw + _i * 8192), 16, 0, 0); } } while (0)
; #define PG8_LDA(dst, b, h) do { if constexpr (!(Sched::CRIP & 4)) _Pragma("unroll") for (int m = 0; m < 4; ++m) dst[m] = PG8_CAT(*(const LAS i32x4*)(lds + PG8_SA(b, h) + aoff + m * 2048), *(const LAS i32x4*)(lds + PG8_SA(b, h) + aoff + m * 2048 + 1024)); } while (0)
; #define PG8_LDB(dst, b, h) do { if constexpr (!(Sched::CRIP & 4)) _Pragma("unroll") for (int n = 0; n < 2; ++n) dst[n] = PG8_CAT(*(const LAS i32x4*)(lds + PG8_SB(b, h) + boff + n * 2048), *(const LAS i32x4*)(lds + PG8_SB(b, h) + boff + n * 2048 + 1024)); } while (0)
; #define PG8_WAIT_V(n) asm volatile("s_waitcnt vmcnt(" #n ")" ::: "memory")
; #define PG8_WAIT_L(n) asm volatile("s_waitcnt lgkmcnt(" #n ")" ::: "memory")
; #define PG8_BAR __builtin_amdgcn_s_barrier()
; #define PG8_SCHED __builtin_amdgcn_sched_barrier(0)
; template <class Epi, class Sched>
; __device__ __forceinline__ void gemm_phase(LAS unsigned char* lds, const Sched& S, const Epi& E) {
;     ...
;             PG8_WAIT_V(8); PG8_WAIT_L(0); PG8_BAR; PG8_MMA(1, 0, At, B0); PG8_MMA(1, 1, At, B1); PG8_BAR2; PG8_SCHED;
;             PG8_LDB(B0, 1, 0); PG8_LDB(B1, 1, 1); PG8_SCHED; PG8_LDA(At, 1, 0); PG8_STAGE(PG8_SA(0, 1), a2, vA[1]);
;             PG8_WAIT_V(8); PG8_WAIT_L(0); PG8_BAR; PG8_MMA(0, 0, At, B0); PG8_MMA(0, 1, At, B1); PG8_BAR2; PG8_SCHED;
	s_setprio 1
	s_waitcnt lgkmcnt(0)
	s_nop 1
	v_mfma_scale_f32_16x16x128_f8f6f4 v[110:113], v[10:17], v[198:205], 0, v185, v185 op_sel_hi:[0,0,0]
	v_mfma_scale_f32_16x16x128_f8f6f4 v[106:109], v[26:33], v[198:205], 0, v185, v185 op_sel_hi:[0,0,0]
	v_mfma_scale_f32_16x16x128_f8f6f4 v[102:105], v[10:17], v[214:221], 0, v185, v185 op_sel_hi:[0,0,0]
	v_mfma_scale_f32_16x16x128_f8f6f4 v[98:101], v[26:33], v[214:221], 0, v185, v185 op_sel_hi:[0,0,0]
	v_mfma_scale_f32_16x16x128_f8f6f4 v[78:81], v[10:17], v[222:229], 0, v185, v185 op_sel_hi:[0,0,0]
	v_mfma_scale_f32_16x16x128_f8f6f4 v[74:77], v[26:33], v[222:229], 0, v185, v185 op_sel_hi:[0,0,0]
	v_mfma_scale_f32_16x16x128_f8f6f4 v[70:73], v[10:17], v[230:237], 0, v185, v185 op_sel_hi:[0,0,0]
	v_mfma_scale_f32_16x16x128_f8f6f4 v[66:69], v[26:33], v[230:237], 0, v185, v185 op_sel_hi:[0,0,0]
	s_setprio 0
	s_setprio 1
	s_nop 1
	v_mfma_scale_f32_16x16x128_f8f6f4 v[94:97], v[2:9], v[198:205], 0, v185, v185 op_sel_hi:[0,0,0]
	v_mfma_scale_f32_16x16x128_f8f6f4 v[90:93], v[18:25], v[198:205], 0, v185, v185 op_sel_hi:[0,0,0]
	v_mfma_scale_f32_16x16x128_f8f6f4 v[86:89], v[2:9], v[214:221], 0, v185, v185 op_sel_hi:[0,0,0]
	v_mfma_scale_f32_16x16x128_f8f6f4 v[82:85], v[18:25], v[214:221], 0, v185, v185 op_sel_hi:[0,0,0]
	v_mfma_scale_f32_16x16x128_f8f6f4 v[62:65], v[2:9], v[222:229], 0, v185, v185 op_sel_hi:[0,0,0]
	v_mfma_scale_f32_16x16x128_f8f6f4 v[58:61], v[18:25], v[222:229], 0, v185, v185 op_sel_hi:[0,0,0]
	v_mfma_scale_f32_16x16x128_f8f6f4 v[54:57], v[2:9], v[230:237], 0, v185, v185 op_sel_hi:[0,0,0]
	v_mfma_scale_f32_16x16x128_f8f6f4 v[50:53], v[18:25], v[230:237], 0, v185, v185 op_sel_hi:[0,0,0]
	s_setprio 0
	s_barrier
	s_add_i32 s40, 0, 0x18000
	s_add_i32 s41, 0, 0x1c000
	v_add_u32_e32 v14, s40, v186
	v_add_u32_e32 v30, s41, v186
	ds_read_b128 v[2:5], v14
	ds_read_b128 v[6:9], v14 offset:1024
	ds_read_b128 v[10:13], v14 offset:2048
	ds_read_b128 v[14:17], v14 offset:3072
	ds_read_b128 v[18:21], v30
	ds_read_b128 v[22:25], v30 offset:1024
	ds_read_b128 v[26:29], v30 offset:2048
	ds_read_b128 v[30:33], v30 offset:3072
	v_mov_b32_e32 v178, v183
	s_mov_b32 m0, s71
	ds_read_b128 v[198:201], v188 offset:32768
	ds_read_b128 v[202:205], v188 offset:33792
	ds_read_b128 v[214:217], v188 offset:34816
	ds_read_b128 v[218:221], v188 offset:35840
	ds_read_b128 v[222:225], v188 offset:36864
	ds_read_b128 v[226:229], v188 offset:37888
	ds_read_b128 v[230:233], v188 offset:38912
	ds_read_b128 v[234:237], v188 offset:39936
	s_nop 0
	global_load_lds_dwordx4 v178, s[34:35]
	v_mov_b32_e32 v178, v184
	s_mov_b32 m0, s72
	s_nop 0
	global_load_lds_dwordx4 v178, s[34:35]
	s_waitcnt vmcnt(8)
	s_waitcnt lgkmcnt(0)
	s_barrier
	s_setprio 1
	s_waitcnt lgkmcnt(0)
	s_nop 1
	v_mfma_scale_f32_16x16x128_f8f6f4 v[174:177], v[2:9], v[198:205], v[174:177], v185, v185 op_sel_hi:[0,0,0]
	v_mfma_scale_f32_16x16x128_f8f6f4 v[170:173], v[10:17], v[198:205], v[170:173], v185, v185 op_sel_hi:[0,0,0]
	v_mfma_scale_f32_16x16x128_f8f6f4 v[166:169], v[2:9], v[214:221], v[166:169], v185, v185 op_sel_hi:[0,0,0]
	v_mfma_scale_f32_16x16x128_f8f6f4 v[162:165], v[10:17], v[214:221], v[162:165], v185, v185 op_sel_hi:[0,0,0]
	v_mfma_scale_f32_16x16x128_f8f6f4 v[142:145], v[2:9], v[222:229], v[142:145], v185, v185 op_sel_hi:[0,0,0]
	v_mfma_scale_f32_16x16x128_f8f6f4 v[138:141], v[10:17], v[222:229], v[138:141], v185, v185 op_sel_hi:[0,0,0]
	v_mfma_scale_f32_16x16x128_f8f6f4 v[134:137], v[2:9], v[230:237], v[134:137], v185, v185 op_sel_hi:[0,0,0]
	v_mfma_scale_f32_16x16x128_f8f6f4 v[130:133], v[10:17], v[230:237], v[130:133], v185, v185 op_sel_hi:[0,0,0]
	s_setprio 0
	s_setprio 1
	s_nop 1
	v_mfma_scale_f32_16x16x128_f8f6f4 v[158:161], v[18:25], v[198:205], v[158:161], v185, v185 op_sel_hi:[0,0,0]
	v_mfma_scale_f32_16x16x128_f8f6f4 v[154:157], v[26:33], v[198:205], v[154:157], v185, v185 op_sel_hi:[0,0,0]
	v_mfma_scale_f32_16x16x128_f8f6f4 v[150:153], v[18:25], v[214:221], v[150:153], v185, v185 op_sel_hi:[0,0,0]
	v_mfma_scale_f32_16x16x128_f8f6f4 v[146:149], v[26:33], v[214:221], v[146:149], v185, v185 op_sel_hi:[0,0,0]
	v_mfma_scale_f32_16x16x128_f8f6f4 v[126:129], v[18:25], v[222:229], v[126:129], v185, v185 op_sel_hi:[0,0,0]
	v_mfma_scale_f32_16x16x128_f8f6f4 v[122:125], v[26:33], v[222:229], v[122:125], v185, v185 op_sel_hi:[0,0,0]
	v_mfma_scale_f32_16x16x128_f8f6f4 v[118:121], v[18:25], v[230:237], v[118:121], v185, v185 op_sel_hi:[0,0,0]
	v_mfma_scale_f32_16x16x128_f8f6f4 v[114:117], v[26:33], v[230:237], v[114:117], v185, v185 op_sel_hi:[0,0,0]
	s_setprio 0
	s_barrier
; #define PG8_STAGE(bufoff, gbase, voff) do { if constexpr (!(Sched::CRIP & 2)) _Pragma("unroll") for (int _i = 0; _i < 2; ++_i) { unsigned _o = (voff)[_i]; asm volatile("" : "+v"(_o)); \
;         __builtin_amdgcn_global_load_lds((const unsigned*)((const char*)(gbase) + _o), (LAS unsigned*)(lds + (bufoff) + ldsw + _i * 8192), 16, 0, 0); } } while (0)
; #define PG8_LDA(dst, b, h) do { if constexpr (!(Sched::CRIP & 4)) _Pragma("unroll") for (int m = 0; m < 4; ++m) dst[m] = PG8_CAT(*(const LAS i32x4*)(lds + PG8_SA(b, h) + aoff + m * 2048), *(const LAS i32x4*)(lds + PG8_SA(b, h) + aoff + m * 2048 + 1024)); } while (0)
; #define PG8_WAIT_V(n) asm volatile("s_waitcnt vmcnt(" #n ")" ::: "memory")
; #define PG8_WAIT_L(n) asm volatile("s_waitcnt lgkmcnt(" #n ")" ::: "memory")
; #define PG8_BAR __builtin_amdgcn_s_barrier()
; #define PG8_SCHED __builtin_amdgcn_sched_barrier(0)
; template <class Epi, class Sched>
; __device__ __forceinline__ void gemm_phase(LAS unsigned char* lds, const Sched& S, const Epi& E) {
;     ...
;             PG8_LDA(At, 1, 1); PG8_STAGE(PG8_SB(1, 0), b3, voffB); PG8_STAGE(PG8_SB(1, 1), b3 + hstep, voffB); PG8_STAGE(PG8_SA(1, 0), a3, vA[0]);
;             PG8_WAIT_V(8); PG8_WAIT_L(0); PG8_BAR; PG8_MMA(1, 0, At, B0); PG8_MMA(1, 1, At, B1); PG8_BAR2; PG8_SCHED;
	v_mov_b32_e32 v178, v1
	s_add_i32 s34, s40, s47
	ds_read_b128 v[198:201], v188 offset:49152
	ds_read_b128 v[202:205], v188 offset:50176
	ds_read_b128 v[214:217], v188 offset:51200
	ds_read_b128 v[218:221], v188 offset:52224
	ds_read_b128 v[222:225], v188 offset:53248
	ds_read_b128 v[226:229], v188 offset:54272
	ds_read_b128 v[230:233], v188 offset:55296
	ds_read_b128 v[234:237], v188 offset:56320
	s_mov_b32 m0, s34
	s_nop 0
	global_load_lds_dwordx4 v178, s[36:37]
	v_mov_b32_e32 v178, v180
	s_add_i32 m0, s34, 0x2000
	s_add_u32 s34, s36, 0x40000
	global_load_lds_dwordx4 v178, s[36:37]
	s_addc_u32 s35, s37, 0
	v_mov_b32_e32 v178, v1
	s_add_i32 s36, s41, s47
	s_mov_b32 m0, s36
	s_nop 0
	global_load_lds_dwordx4 v178, s[34:35]
	v_mov_b32_e32 v178, v180
	s_add_i32 m0, s36, 0x2000
	s_nop 0
	global_load_lds_dwordx4 v178, s[34:35]
	v_mov_b32_e32 v178, v181
	s_mov_b32 m0, s74
	s_nop 0
	global_load_lds_dwordx4 v178, s[30:31]
	v_mov_b32_e32 v178, v182
	s_mov_b32 m0, s75
	s_nop 0
	global_load_lds_dwordx4 v178, s[30:31]
	s_waitcnt vmcnt(8)
	s_waitcnt lgkmcnt(0)
	s_barrier
	s_setprio 1
	s_waitcnt lgkmcnt(0)
	s_nop 1
	v_mfma_scale_f32_16x16x128_f8f6f4 v[110:113], v[2:9], v[198:205], v[110:113], v185, v185 op_sel_hi:[0,0,0]
	v_mfma_scale_f32_16x16x128_f8f6f4 v[106:109], v[10:17], v[198:205], v[106:109], v185, v185 op_sel_hi:[0,0,0]
	v_mfma_scale_f32_16x16x128_f8f6f4 v[102:105], v[2:9], v[214:221], v[102:105], v185, v185 op_sel_hi:[0,0,0]
	v_mfma_scale_f32_16x16x128_f8f6f4 v[98:101], v[10:17], v[214:221], v[98:101], v185, v185 op_sel_hi:[0,0,0]
	v_mfma_scale_f32_16x16x128_f8f6f4 v[78:81], v[2:9], v[222:229], v[78:81], v185, v185 op_sel_hi:[0,0,0]
	v_mfma_scale_f32_16x16x128_f8f6f4 v[74:77], v[10:17], v[222:229], v[74:77], v185, v185 op_sel_hi:[0,0,0]
	v_mfma_scale_f32_16x16x128_f8f6f4 v[70:73], v[2:9], v[230:237], v[70:73], v185, v185 op_sel_hi:[0,0,0]
	v_mfma_scale_f32_16x16x128_f8f6f4 v[66:69], v[10:17], v[230:237], v[66:69], v185, v185 op_sel_hi:[0,0,0]
	s_setprio 0
	s_setprio 1
	s_nop 1
	v_mfma_scale_f32_16x16x128_f8f6f4 v[94:97], v[18:25], v[198:205], v[94:97], v185, v185 op_sel_hi:[0,0,0]
	v_mfma_scale_f32_16x16x128_f8f6f4 v[90:93], v[26:33], v[198:205], v[90:93], v185, v185 op_sel_hi:[0,0,0]
	v_mfma_scale_f32_16x16x128_f8f6f4 v[86:89], v[18:25], v[214:221], v[86:89], v185, v185 op_sel_hi:[0,0,0]
	v_mfma_scale_f32_16x16x128_f8f6f4 v[82:85], v[26:33], v[214:221], v[82:85], v185, v185 op_sel_hi:[0,0,0]
	v_mfma_scale_f32_16x16x128_f8f6f4 v[62:65], v[18:25], v[222:229], v[62:65], v185, v185 op_sel_hi:[0,0,0]
	v_mfma_scale_f32_16x16x128_f8f6f4 v[58:61], v[26:33], v[222:229], v[58:61], v185, v185 op_sel_hi:[0,0,0]
	v_mfma_scale_f32_16x16x128_f8f6f4 v[54:57], v[18:25], v[230:237], v[54:57], v185, v185 op_sel_hi:[0,0,0]
	v_mfma_scale_f32_16x16x128_f8f6f4 v[50:53], v[26:33], v[230:237], v[50:53], v185, v185 op_sel_hi:[0,0,0]
	s_setprio 0
	s_barrier
	s_add_i32 s84, s84, 2
	s_addk_i32 s83, 0x100

; __device__ __forceinline__ float sat8(float x) { return __builtin_amdgcn_fmed3f(x, -448.0f, 448.0f); }
; __device__ __forceinline__ unsigned pk4_fp8(float a, float b, float c, float d) { int v = 0; v = __builtin_amdgcn_cvt_pk_fp8_f32(a, b, v, false); v = __builtin_amdgcn_cvt_pk_fp8_f32(c, d, v, true); return (unsigned)v; }
;     __device__ __forceinline__ void operator()(const f32x4 (&acc)[2][2][4][2], const pg8::Unit& u, const Pre& q, int wr, int wc, int fr, int fq) const {
;         const int rl0 = wr * 64 + fr, colw = u.pn * 256 + wc * 32;
;         constexpr float DS = 1.0f / (FP8_SH * FP8_SW);
; #pragma unroll
;         for (int ai = 0; ai < 2; ++ai)
; #pragma unroll
;             for (int mp = 0; mp < 2; ++mp)
; #pragma unroll
;                 for (int bj = 0; bj < 2; ++bj) { unsigned lo[2], hi[2];
; #pragma unroll
;                     for (int mm = 0; mm < 2; ++mm) { const int m = 2 * mp + mm; const float gt = q.gt[ai][m] * FP8_SY;
;                         const f32x4 v0 = (acc[ai][bj][m][0] * DS + q.bv[bj][0]) * gt, v1 = (acc[ai][bj][m][1] * DS + q.bv[bj][1]) * gt;
;                         lo[mm] = pk4_fp8(sat8(v0[0]), sat8(v0[1]), sat8(v0[2]), sat8(v0[3])); hi[mm] = pk4_fp8(sat8(v1[0]), sat8(v1[1]), sat8(v1[2]), sat8(v1[3])); }
;                     const v2u r0 = __builtin_amdgcn_permlane16_swap(lo[0], lo[1], false, false), r1 = __builtin_amdgcn_permlane16_swap(hi[0], hi[1], false, false);
;                     unsigned char* rowp = y2 + (size_t)(u.pm * 256 + rl0 + ai * 128 + (2 * mp + (fq & 1)) * 16) * D + colw + bj * 128 + 16 * (fq >> 1);
;                     *(v4u*)rowp = (v4u){r0.x, r1.x, r0.y, r1.y}; }
.LBB0_810:
	v_mov_b32_e32 v3, v0
	s_lshl_b32 s24, s24, 8
	v_readfirstlane_b32 s15, v3
	s_ashr_i32 s17, s15, 2
	s_lshr_b32 s15, s15, 1
	s_and_b32 s15, s15, 0x60
	s_andn2_b32 s17, s17, 63
	s_or_b32 s24, s15, s24
	s_lshl_b32 s15, s22, 8
	s_add_i32 s17, s17, s15
	v_and_or_b32 v2, v3, 31, s17
	v_lshrrev_b32_e32 v3, 1, v3
	s_waitcnt vmcnt(8)
	v_mul_f32_e32 v10, 0x42000000, v197
	v_pk_fma_f32 v[4:5], v[176:177], s[10:11], v[48:49] op_sel_hi:[1,0,1]
	v_pk_fma_f32 v[6:7], v[174:175], s[10:11], v[46:47] op_sel_hi:[1,0,1]
	v_and_b32_e32 v178, 16, v3
	v_ashrrev_i32_e32 v3, 31, v2
	v_pk_mul_f32 v[4:5], v[10:11], v[4:5] op_sel_hi:[0,1]
	v_pk_mul_f32 v[6:7], v[10:11], v[6:7] op_sel_hi:[0,1]
	v_pk_fma_f32 v[14:15], v[170:171], s[10:11], v[42:43] op_sel_hi:[1,0,1]
	v_lshlrev_b64 v[8:9], 11, v[2:3]
	v_pk_fma_f32 v[12:13], v[172:173], s[10:11], v[44:45] op_sel_hi:[1,0,1]
	v_pk_mul_f32 v[14:15], v[10:11], v[14:15] op_sel_hi:[0,1]
	v_med3_f32 v3, v6, s79, v189
	v_med3_f32 v6, v7, s79, v189
	v_med3_f32 v7, v4, s79, v189
	v_mov_b32_e32 v4, v179
	v_pk_mul_f32 v[12:13], v[10:11], v[12:13] op_sel_hi:[0,1]
	v_med3_f32 v11, v5, s79, v189
	v_cvt_pk_fp8_f32 v4, v3, v6
	v_med3_f32 v3, v14, s79, v189
	v_med3_f32 v6, v15, s79, v189
	v_mov_b32_e32 v5, v179
	v_cvt_pk_fp8_f32 v5, v3, v6
	v_med3_f32 v3, v12, s79, v189
	v_med3_f32 v6, v13, s79, v189
	v_cvt_pk_fp8_f32 v4, v7, v11 op_sel:[0,0,1]
	v_cvt_pk_fp8_f32 v5, v3, v6 op_sel:[0,0,1]
	v_mul_f32_e32 v12, 0x42000000, v196
	v_pk_fma_f32 v[6:7], v[168:169], s[10:11], v[48:49] op_sel_hi:[1,0,1]
	v_pk_fma_f32 v[14:15], v[166:167], s[10:11], v[46:47] op_sel_hi:[1,0,1]
	v_pk_mul_f32 v[6:7], v[12:13], v[6:7] op_sel_hi:[0,1]
	v_pk_mul_f32 v[14:15], v[12:13], v[14:15] op_sel_hi:[0,1]
	v_pk_fma_f32 v[16:17], v[164:165], s[10:11], v[44:45] op_sel_hi:[1,0,1]
	v_pk_fma_f32 v[18:19], v[162:163], s[10:11], v[42:43] op_sel_hi:[1,0,1]
	v_pk_mul_f32 v[16:17], v[12:13], v[16:17] op_sel_hi:[0,1]
	v_pk_mul_f32 v[18:19], v[12:13], v[18:19] op_sel_hi:[0,1]
	v_med3_f32 v3, v14, s79, v189
	v_med3_f32 v11, v15, s79, v189
	v_med3_f32 v13, v6, s79, v189
	v_mov_b32_e32 v6, v179
	v_med3_f32 v14, v7, s79, v189
	v_cvt_pk_fp8_f32 v6, v3, v11
	v_med3_f32 v3, v18, s79, v189
	v_med3_f32 v11, v19, s79, v189
	v_mov_b32_e32 v7, v179
	v_cvt_pk_fp8_f32 v7, v3, v11
	v_med3_f32 v3, v16, s79, v189
	v_med3_f32 v11, v17, s79, v189
	v_cvt_pk_fp8_f32 v6, v13, v14 op_sel:[0,0,1]
	v_cvt_pk_fp8_f32 v7, v3, v11 op_sel:[0,0,1]
	s_ashr_i32 s25, s24, 31
	v_lshl_add_u64 v[8:9], s[6:7], 0, v[8:9]
	v_lshl_add_u64 v[8:9], v[8:9], 0, s[24:25]
	v_permlane16_swap_b32_e32 v4, v6
	v_permlane16_swap_b32_e32 v5, v7
	v_lshl_add_u64 v[8:9], v[8:9], 0, v[178:179]
	global_store_dwordx4 v[8:9], v[4:7], off
	v_pk_fma_f32 v[14:15], v[156:157], s[10:11], v[36:37] op_sel_hi:[1,0,1]
	v_pk_fma_f32 v[16:17], v[154:155], s[10:11], v[34:35] op_sel_hi:[1,0,1]
	v_pk_fma_f32 v[4:5], v[160:161], s[10:11], v[40:41] op_sel_hi:[1,0,1]
	v_pk_fma_f32 v[6:7], v[158:159], s[10:11], v[38:39] op_sel_hi:[1,0,1]
	v_pk_mul_f32 v[4:5], v[10:11], v[4:5] op_sel_hi:[0,1]
	v_pk_mul_f32 v[6:7], v[10:11], v[6:7] op_sel_hi:[0,1]
	v_pk_mul_f32 v[14:15], v[10:11], v[14:15] op_sel_hi:[0,1]
	v_pk_mul_f32 v[10:11], v[10:11], v[16:17] op_sel_hi:[0,1]
	v_med3_f32 v3, v6, s79, v189
	v_med3_f32 v6, v7, s79, v189
	v_med3_f32 v7, v4, s79, v189
	v_mov_b32_e32 v4, v179
	v_med3_f32 v13, v5, s79, v189
	v_cvt_pk_fp8_f32 v4, v3, v6
	v_med3_f32 v3, v10, s79, v189
	v_med3_f32 v6, v11, s79, v189
	v_mov_b32_e32 v5, v179
	v_cvt_pk_fp8_f32 v5, v3, v6
	v_med3_f32 v3, v14, s79, v189
	v_med3_f32 v6, v15, s79, v189
	v_cvt_pk_fp8_f32 v4, v7, v13 op_sel:[0,0,1]
	v_cvt_pk_fp8_f32 v5, v3, v6 op_sel:[0,0,1]
	v_pk_fma_f32 v[6:7], v[152:153], s[10:11], v[40:41] op_sel_hi:[1,0,1]
	v_pk_fma_f32 v[10:11], v[150:151], s[10:11], v[38:39] op_sel_hi:[1,0,1]
	v_pk_mul_f32 v[6:7], v[12:13], v[6:7] op_sel_hi:[0,1]
	v_pk_mul_f32 v[10:11], v[12:13], v[10:11] op_sel_hi:[0,1]
	v_pk_fma_f32 v[14:15], v[148:149], s[10:11], v[36:37] op_sel_hi:[1,0,1]
	v_pk_fma_f32 v[16:17], v[146:147], s[10:11], v[34:35] op_sel_hi:[1,0,1]
	v_pk_mul_f32 v[14:15], v[12:13], v[14:15] op_sel_hi:[0,1]
	v_pk_mul_f32 v[12:13], v[12:13], v[16:17] op_sel_hi:[0,1]
	v_med3_f32 v3, v10, s79, v189
	v_med3_f32 v10, v11, s79, v189
	v_med3_f32 v11, v6, s79, v189
	v_mov_b32_e32 v6, v179
	v_med3_f32 v16, v7, s79, v189
	v_cvt_pk_fp8_f32 v6, v3, v10
	v_med3_f32 v3, v12, s79, v189
	v_med3_f32 v10, v13, s79, v189
	v_mov_b32_e32 v7, v179
	v_cvt_pk_fp8_f32 v7, v3, v10
	v_med3_f32 v3, v14, s79, v189
	v_med3_f32 v10, v15, s79, v189
	v_cvt_pk_fp8_f32 v6, v11, v16 op_sel:[0,0,1]
	v_cvt_pk_fp8_f32 v7, v3, v10 op_sel:[0,0,1]
	v_mul_f32_e32 v10, 0x42000000, v195
	v_pk_fma_f32 v[14:15], v[138:139], s[10:11], v[42:43] op_sel_hi:[1,0,1]
	v_permlane16_swap_b32_e32 v4, v6
	v_permlane16_swap_b32_e32 v5, v7
	global_store_dwordx4 v[8:9], v[4:7], off offset:128
	v_pk_fma_f32 v[12:13], v[140:141], s[10:11], v[44:45] op_sel_hi:[1,0,1]
	v_pk_mul_f32 v[14:15], v[10:11], v[14:15] op_sel_hi:[0,1]
	v_or_b32_e32 v4, 32, v2
	v_ashrrev_i32_e32 v5, 31, v4
	v_lshlrev_b64 v[8:9], 11, v[4:5]
	v_pk_fma_f32 v[4:5], v[144:145], s[10:11], v[48:49] op_sel_hi:[1,0,1]
	v_pk_fma_f32 v[6:7], v[142:143], s[10:11], v[46:47] op_sel_hi:[1,0,1]
	v_pk_mul_f32 v[4:5], v[10:11], v[4:5] op_sel_hi:[0,1]
	v_pk_mul_f32 v[6:7], v[10:11], v[6:7] op_sel_hi:[0,1]
	v_med3_f32 v3, v6, s79, v189
	v_med3_f32 v6, v7, s79, v189
	v_med3_f32 v7, v4, s79, v189
	v_mov_b32_e32 v4, v179
	v_pk_mul_f32 v[12:13], v[10:11], v[12:13] op_sel_hi:[0,1]
	v_med3_f32 v11, v5, s79, v189
	v_cvt_pk_fp8_f32 v4, v3, v6
	v_med3_f32 v3, v14, s79, v189
	v_med3_f32 v6, v15, s79, v189
	v_mov_b32_e32 v5, v179
; __device__ __forceinline__ float sat8(float x) { return __builtin_amdgcn_fmed3f(x, -448.0f, 448.0f); }
; __device__ __forceinline__ unsigned pk4_fp8(float a, float b, float c, float d) { int v = 0; v = __builtin_amdgcn_cvt_pk_fp8_f32(a, b, v, false); v = __builtin_amdgcn_cvt_pk_fp8_f32(c, d, v, true); return (unsigned)v; }
;     __device__ __forceinline__ void operator()(const f32x4 (&acc)[2][2][4][2], const pg8::Unit& u, const Pre& q, int wr, int wc, int fr, int fq) const {
;     ...
;                 for (int bj = 0; bj < 2; ++bj) { unsigned lo[2], hi[2];
; #pragma unroll
;                     for (int mm = 0; mm < 2; ++mm) { const int m = 2 * mp + mm; const float gt = q.gt[ai][m] * FP8_SY;
;                         const f32x4 v0 = (acc[ai][bj][m][0] * DS + q.bv[bj][0]) * gt, v1 = (acc[ai][bj][m][1] * DS + q.bv[bj][1]) * gt;
;                         lo[mm] = pk4_fp8(sat8(v0[0]), sat8(v0[1]), sat8(v0[2]), sat8(v0[3])); hi[mm] = pk4_fp8(sat8(v1[0]), sat8(v1[1]), sat8(v1[2]), sat8(v1[3])); }
;                     const v2u r0 = __builtin_amdgcn_permlane16_swap(lo[0], lo[1], false, false), r1 = __builtin_amdgcn_permlane16_swap(hi[0], hi[1], false, false);
;                     unsigned char* rowp = y2 + (size_t)(u.pm * 256 + rl0 + ai * 128 + (2 * mp + (fq & 1)) * 16) * D + colw + bj * 128 + 16 * (fq >> 1);
;                     *(v4u*)rowp = (v4u){r0.x, r1.x, r0.y, r1.y}; }
	v_cvt_pk_fp8_f32 v5, v3, v6
	v_med3_f32 v3, v12, s79, v189
	v_med3_f32 v6, v13, s79, v189
	v_cvt_pk_fp8_f32 v4, v7, v11 op_sel:[0,0,1]
	v_cvt_pk_fp8_f32 v5, v3, v6 op_sel:[0,0,1]
	v_mul_f32_e32 v12, 0x42000000, v194
	v_pk_fma_f32 v[6:7], v[136:137], s[10:11], v[48:49] op_sel_hi:[1,0,1]
	v_pk_fma_f32 v[14:15], v[134:135], s[10:11], v[46:47] op_sel_hi:[1,0,1]
	v_pk_mul_f32 v[6:7], v[12:13], v[6:7] op_sel_hi:[0,1]
	v_pk_mul_f32 v[14:15], v[12:13], v[14:15] op_sel_hi:[0,1]
	v_pk_fma_f32 v[16:17], v[132:133], s[10:11], v[44:45] op_sel_hi:[1,0,1]
	v_pk_fma_f32 v[18:19], v[130:131], s[10:11], v[42:43] op_sel_hi:[1,0,1]
	v_pk_mul_f32 v[16:17], v[12:13], v[16:17] op_sel_hi:[0,1]
	v_pk_mul_f32 v[18:19], v[12:13], v[18:19] op_sel_hi:[0,1]
	v_med3_f32 v3, v14, s79, v189
	v_med3_f32 v11, v15, s79, v189
	v_med3_f32 v13, v6, s79, v189
	v_mov_b32_e32 v6, v179
	v_med3_f32 v14, v7, s79, v189
	v_cvt_pk_fp8_f32 v6, v3, v11
	v_med3_f32 v3, v18, s79, v189
	v_med3_f32 v11, v19, s79, v189
	v_mov_b32_e32 v7, v179
	v_cvt_pk_fp8_f32 v7, v3, v11
	v_med3_f32 v3, v16, s79, v189
	v_med3_f32 v11, v17, s79, v189
	v_cvt_pk_fp8_f32 v6, v13, v14 op_sel:[0,0,1]
	v_cvt_pk_fp8_f32 v7, v3, v11 op_sel:[0,0,1]
	v_lshl_add_u64 v[8:9], s[6:7], 0, v[8:9]
	v_lshl_add_u64 v[8:9], v[8:9], 0, s[24:25]
	v_permlane16_swap_b32_e32 v4, v6
	v_permlane16_swap_b32_e32 v5, v7
	v_lshl_add_u64 v[8:9], v[8:9], 0, v[178:179]
	global_store_dwordx4 v[8:9], v[4:7], off
	v_pk_fma_f32 v[14:15], v[124:125], s[10:11], v[36:37] op_sel_hi:[1,0,1]
	v_pk_fma_f32 v[16:17], v[122:123], s[10:11], v[34:35] op_sel_hi:[1,0,1]
	v_pk_fma_f32 v[4:5], v[128:129], s[10:11], v[40:41] op_sel_hi:[1,0,1]
	v_pk_fma_f32 v[6:7], v[126:127], s[10:11], v[38:39] op_sel_hi:[1,0,1]
	v_pk_mul_f32 v[4:5], v[10:11], v[4:5] op_sel_hi:[0,1]
	v_pk_mul_f32 v[6:7], v[10:11], v[6:7] op_sel_hi:[0,1]
	v_pk_mul_f32 v[14:15], v[10:11], v[14:15] op_sel_hi:[0,1]
	v_pk_mul_f32 v[10:11], v[10:11], v[16:17] op_sel_hi:[0,1]
	v_med3_f32 v3, v6, s79, v189
	v_med3_f32 v6, v7, s79, v189
	v_med3_f32 v7, v4, s79, v189
	v_mov_b32_e32 v4, v179
	v_med3_f32 v13, v5, s79, v189
	v_cvt_pk_fp8_f32 v4, v3, v6
	v_med3_f32 v3, v10, s79, v189
	v_med3_f32 v6, v11, s79, v189
	v_mov_b32_e32 v5, v179
	v_cvt_pk_fp8_f32 v5, v3, v6
	v_med3_f32 v3, v14, s79, v189
	v_med3_f32 v6, v15, s79, v189
	v_cvt_pk_fp8_f32 v4, v7, v13 op_sel:[0,0,1]
	v_cvt_pk_fp8_f32 v5, v3, v6 op_sel:[0,0,1]
	v_pk_fma_f32 v[6:7], v[120:121], s[10:11], v[40:41] op_sel_hi:[1,0,1]
	v_pk_fma_f32 v[10:11], v[118:119], s[10:11], v[38:39] op_sel_hi:[1,0,1]
	v_pk_mul_f32 v[6:7], v[12:13], v[6:7] op_sel_hi:[0,1]
	v_pk_mul_f32 v[10:11], v[12:13], v[10:11] op_sel_hi:[0,1]
	v_pk_fma_f32 v[14:15], v[116:117], s[10:11], v[36:37] op_sel_hi:[1,0,1]
	v_pk_fma_f32 v[16:17], v[114:115], s[10:11], v[34:35] op_sel_hi:[1,0,1]
	v_pk_mul_f32 v[14:15], v[12:13], v[14:15] op_sel_hi:[0,1]
	v_pk_mul_f32 v[12:13], v[12:13], v[16:17] op_sel_hi:[0,1]
	v_med3_f32 v3, v10, s79, v189
	v_med3_f32 v10, v11, s79, v189
	v_med3_f32 v11, v6, s79, v189
	v_mov_b32_e32 v6, v179
	v_med3_f32 v16, v7, s79, v189
	v_cvt_pk_fp8_f32 v6, v3, v10
	v_med3_f32 v3, v12, s79, v189
	v_med3_f32 v10, v13, s79, v189
	v_mov_b32_e32 v7, v179
	v_cvt_pk_fp8_f32 v7, v3, v10
	v_med3_f32 v3, v14, s79, v189
	v_med3_f32 v10, v15, s79, v189
	v_cvt_pk_fp8_f32 v6, v11, v16 op_sel:[0,0,1]
	v_cvt_pk_fp8_f32 v7, v3, v10 op_sel:[0,0,1]
	v_mul_f32_e32 v10, 0x42000000, v193
	v_pk_fma_f32 v[14:15], v[106:107], s[10:11], v[42:43] op_sel_hi:[1,0,1]
	v_permlane16_swap_b32_e32 v4, v6
	v_permlane16_swap_b32_e32 v5, v7
	global_store_dwordx4 v[8:9], v[4:7], off offset:128
	v_pk_fma_f32 v[12:13], v[108:109], s[10:11], v[44:45] op_sel_hi:[1,0,1]
	v_pk_mul_f32 v[14:15], v[10:11], v[14:15] op_sel_hi:[0,1]
	v_add_u32_e32 v4, 0x80, v2
	v_ashrrev_i32_e32 v5, 31, v4
	v_lshlrev_b64 v[8:9], 11, v[4:5]
	v_pk_fma_f32 v[4:5], v[112:113], s[10:11], v[48:49] op_sel_hi:[1,0,1]
	v_pk_fma_f32 v[6:7], v[110:111], s[10:11], v[46:47] op_sel_hi:[1,0,1]
	v_pk_mul_f32 v[4:5], v[10:11], v[4:5] op_sel_hi:[0,1]
	v_pk_mul_f32 v[6:7], v[10:11], v[6:7] op_sel_hi:[0,1]
	v_med3_f32 v3, v6, s79, v189
	v_med3_f32 v6, v7, s79, v189
	v_med3_f32 v7, v4, s79, v189
	v_mov_b32_e32 v4, v179
	v_pk_mul_f32 v[12:13], v[10:11], v[12:13] op_sel_hi:[0,1]
	v_med3_f32 v11, v5, s79, v189
	v_cvt_pk_fp8_f32 v4, v3, v6
	v_med3_f32 v3, v14, s79, v189
	v_med3_f32 v6, v15, s79, v189
	v_mov_b32_e32 v5, v179
	v_cvt_pk_fp8_f32 v5, v3, v6
	v_med3_f32 v3, v12, s79, v189
	v_med3_f32 v6, v13, s79, v189
	v_cvt_pk_fp8_f32 v4, v7, v11 op_sel:[0,0,1]
	v_cvt_pk_fp8_f32 v5, v3, v6 op_sel:[0,0,1]
	v_mul_f32_e32 v12, 0x42000000, v192
	v_pk_fma_f32 v[6:7], v[104:105], s[10:11], v[48:49] op_sel_hi:[1,0,1]
	v_pk_fma_f32 v[14:15], v[102:103], s[10:11], v[46:47] op_sel_hi:[1,0,1]
	v_pk_mul_f32 v[6:7], v[12:13], v[6:7] op_sel_hi:[0,1]
	v_pk_mul_f32 v[14:15], v[12:13], v[14:15] op_sel_hi:[0,1]
	v_pk_fma_f32 v[16:17], v[100:101], s[10:11], v[44:45] op_sel_hi:[1,0,1]
	v_pk_fma_f32 v[18:19], v[98:99], s[10:11], v[42:43] op_sel_hi:[1,0,1]
	v_pk_mul_f32 v[16:17], v[12:13], v[16:17] op_sel_hi:[0,1]
	v_pk_mul_f32 v[18:19], v[12:13], v[18:19] op_sel_hi:[0,1]
	v_med3_f32 v3, v14, s79, v189
	v_med3_f32 v11, v15, s79, v189
	v_med3_f32 v13, v6, s79, v189
	v_mov_b32_e32 v6, v179
	v_med3_f32 v14, v7, s79, v189
	v_cvt_pk_fp8_f32 v6, v3, v11
	v_med3_f32 v3, v18, s79, v189
	v_med3_f32 v11, v19, s79, v189
	v_mov_b32_e32 v7, v179
	v_cvt_pk_fp8_f32 v7, v3, v11
	v_med3_f32 v3, v16, s79, v189
	v_med3_f32 v11, v17, s79, v189
	v_cvt_pk_fp8_f32 v6, v13, v14 op_sel:[0,0,1]
	v_cvt_pk_fp8_f32 v7, v3, v11 op_sel:[0,0,1]
	v_lshl_add_u64 v[8:9], s[6:7], 0, v[8:9]
	v_lshl_add_u64 v[8:9], v[8:9], 0, s[24:25]
; __device__ __forceinline__ float sat8(float x) { return __builtin_amdgcn_fmed3f(x, -448.0f, 448.0f); }
; __device__ __forceinline__ unsigned pk4_fp8(float a, float b, float c, float d) { int v = 0; v = __builtin_amdgcn_cvt_pk_fp8_f32(a, b, v, false); v = __builtin_amdgcn_cvt_pk_fp8_f32(c, d, v, true); return (unsigned)v; }
;     __device__ __forceinline__ void operator()(const f32x4 (&acc)[2][2][4][2], const pg8::Unit& u, const Pre& q, int wr, int wc, int fr, int fq) const {
;     ...
;                 for (int bj = 0; bj < 2; ++bj) { unsigned lo[2], hi[2];
; #pragma unroll
;                     for (int mm = 0; mm < 2; ++mm) { const int m = 2 * mp + mm; const float gt = q.gt[ai][m] * FP8_SY;
;                         const f32x4 v0 = (acc[ai][bj][m][0] * DS + q.bv[bj][0]) * gt, v1 = (acc[ai][bj][m][1] * DS + q.bv[bj][1]) * gt;
;                         lo[mm] = pk4_fp8(sat8(v0[0]), sat8(v0[1]), sat8(v0[2]), sat8(v0[3])); hi[mm] = pk4_fp8(sat8(v1[0]), sat8(v1[1]), sat8(v1[2]), sat8(v1[3])); }
;                     const v2u r0 = __builtin_amdgcn_permlane16_swap(lo[0], lo[1], false, false), r1 = __builtin_amdgcn_permlane16_swap(hi[0], hi[1], false, false);
;                     unsigned char* rowp = y2 + (size_t)(u.pm * 256 + rl0 + ai * 128 + (2 * mp + (fq & 1)) * 16) * D + colw + bj * 128 + 16 * (fq >> 1);
;                     *(v4u*)rowp = (v4u){r0.x, r1.x, r0.y, r1.y}; }
	v_permlane16_swap_b32_e32 v4, v6
	v_permlane16_swap_b32_e32 v5, v7
	v_lshl_add_u64 v[8:9], v[8:9], 0, v[178:179]
	global_store_dwordx4 v[8:9], v[4:7], off
	v_pk_fma_f32 v[14:15], v[92:93], s[10:11], v[36:37] op_sel_hi:[1,0,1]
	v_pk_fma_f32 v[16:17], v[90:91], s[10:11], v[34:35] op_sel_hi:[1,0,1]
	v_pk_fma_f32 v[4:5], v[96:97], s[10:11], v[40:41] op_sel_hi:[1,0,1]
	v_pk_fma_f32 v[6:7], v[94:95], s[10:11], v[38:39] op_sel_hi:[1,0,1]
	v_pk_mul_f32 v[4:5], v[10:11], v[4:5] op_sel_hi:[0,1]
	v_pk_mul_f32 v[6:7], v[10:11], v[6:7] op_sel_hi:[0,1]
	v_pk_mul_f32 v[14:15], v[10:11], v[14:15] op_sel_hi:[0,1]
	v_pk_mul_f32 v[10:11], v[10:11], v[16:17] op_sel_hi:[0,1]
	v_med3_f32 v3, v6, s79, v189
	v_med3_f32 v6, v7, s79, v189
	v_med3_f32 v7, v4, s79, v189
	v_mov_b32_e32 v4, v179
	v_med3_f32 v13, v5, s79, v189
	v_cvt_pk_fp8_f32 v4, v3, v6
	v_med3_f32 v3, v10, s79, v189
	v_med3_f32 v6, v11, s79, v189
	v_mov_b32_e32 v5, v179
	v_cvt_pk_fp8_f32 v5, v3, v6
	v_med3_f32 v3, v14, s79, v189
	v_med3_f32 v6, v15, s79, v189
	v_cvt_pk_fp8_f32 v4, v7, v13 op_sel:[0,0,1]
	v_cvt_pk_fp8_f32 v5, v3, v6 op_sel:[0,0,1]
	v_pk_fma_f32 v[6:7], v[88:89], s[10:11], v[40:41] op_sel_hi:[1,0,1]
	v_pk_fma_f32 v[10:11], v[86:87], s[10:11], v[38:39] op_sel_hi:[1,0,1]
	v_pk_mul_f32 v[6:7], v[12:13], v[6:7] op_sel_hi:[0,1]
	v_pk_mul_f32 v[10:11], v[12:13], v[10:11] op_sel_hi:[0,1]
	v_pk_fma_f32 v[14:15], v[84:85], s[10:11], v[36:37] op_sel_hi:[1,0,1]
	v_pk_fma_f32 v[16:17], v[82:83], s[10:11], v[34:35] op_sel_hi:[1,0,1]
	v_pk_mul_f32 v[14:15], v[12:13], v[14:15] op_sel_hi:[0,1]
	v_pk_mul_f32 v[12:13], v[12:13], v[16:17] op_sel_hi:[0,1]
	v_med3_f32 v3, v10, s79, v189
	v_med3_f32 v10, v11, s79, v189
	v_med3_f32 v11, v6, s79, v189
	v_mov_b32_e32 v6, v179
	v_med3_f32 v16, v7, s79, v189
	v_cvt_pk_fp8_f32 v6, v3, v10
	v_med3_f32 v3, v12, s79, v189
	v_med3_f32 v10, v13, s79, v189
	v_mov_b32_e32 v7, v179
	v_cvt_pk_fp8_f32 v7, v3, v10
	v_med3_f32 v3, v14, s79, v189
	v_med3_f32 v10, v15, s79, v189
	v_cvt_pk_fp8_f32 v6, v11, v16 op_sel:[0,0,1]
	v_cvt_pk_fp8_f32 v7, v3, v10 op_sel:[0,0,1]
	v_add_u32_e32 v2, 0xa0, v2
	v_ashrrev_i32_e32 v3, 31, v2
	v_permlane16_swap_b32_e32 v4, v6
	v_permlane16_swap_b32_e32 v5, v7
	global_store_dwordx4 v[8:9], v[4:7], off offset:128
	v_mul_f32_e32 v8, 0x42000000, v191
	v_pk_fma_f32 v[10:11], v[76:77], s[10:11], v[44:45] op_sel_hi:[1,0,1]
	v_lshlrev_b64 v[6:7], 11, v[2:3]
	v_pk_fma_f32 v[2:3], v[80:81], s[10:11], v[48:49] op_sel_hi:[1,0,1]
	v_pk_fma_f32 v[4:5], v[78:79], s[10:11], v[46:47] op_sel_hi:[1,0,1]
	v_pk_mul_f32 v[2:3], v[8:9], v[2:3] op_sel_hi:[0,1]
	v_pk_mul_f32 v[4:5], v[8:9], v[4:5] op_sel_hi:[0,1]
	v_pk_fma_f32 v[12:13], v[74:75], s[10:11], v[42:43] op_sel_hi:[1,0,1]
	v_pk_mul_f32 v[10:11], v[8:9], v[10:11] op_sel_hi:[0,1]
	v_pk_mul_f32 v[12:13], v[8:9], v[12:13] op_sel_hi:[0,1]
	v_med3_f32 v4, v4, s79, v189
	v_med3_f32 v5, v5, s79, v189
	v_med3_f32 v9, v2, s79, v189
	v_mov_b32_e32 v2, v179
	v_med3_f32 v14, v3, s79, v189
	v_cvt_pk_fp8_f32 v2, v4, v5
	v_med3_f32 v4, v12, s79, v189
	v_med3_f32 v5, v13, s79, v189
	v_mov_b32_e32 v3, v179
	v_cvt_pk_fp8_f32 v3, v4, v5
	v_med3_f32 v4, v10, s79, v189
	v_med3_f32 v5, v11, s79, v189
	v_mul_f32_e32 v10, 0x42000000, v190
	v_cvt_pk_fp8_f32 v3, v4, v5 op_sel:[0,0,1]
	v_pk_fma_f32 v[4:5], v[72:73], s[10:11], v[48:49] op_sel_hi:[1,0,1]
	v_pk_fma_f32 v[12:13], v[70:71], s[10:11], v[46:47] op_sel_hi:[1,0,1]
	v_cvt_pk_fp8_f32 v2, v9, v14 op_sel:[0,0,1]
	v_pk_mul_f32 v[4:5], v[10:11], v[4:5] op_sel_hi:[0,1]
	v_pk_mul_f32 v[12:13], v[10:11], v[12:13] op_sel_hi:[0,1]
	v_pk_fma_f32 v[14:15], v[68:69], s[10:11], v[44:45] op_sel_hi:[1,0,1]
	v_pk_fma_f32 v[16:17], v[66:67], s[10:11], v[42:43] op_sel_hi:[1,0,1]
	v_pk_mul_f32 v[14:15], v[10:11], v[14:15] op_sel_hi:[0,1]
	v_pk_mul_f32 v[16:17], v[10:11], v[16:17] op_sel_hi:[0,1]
	v_med3_f32 v9, v12, s79, v189
	v_med3_f32 v11, v13, s79, v189
	v_med3_f32 v12, v4, s79, v189
	v_mov_b32_e32 v4, v179
	v_med3_f32 v13, v5, s79, v189
	v_cvt_pk_fp8_f32 v4, v9, v11
	v_med3_f32 v9, v16, s79, v189
	v_med3_f32 v11, v17, s79, v189
	v_mov_b32_e32 v5, v179
	v_cvt_pk_fp8_f32 v5, v9, v11
	v_med3_f32 v9, v14, s79, v189
	v_med3_f32 v11, v15, s79, v189
	v_cvt_pk_fp8_f32 v4, v12, v13 op_sel:[0,0,1]
	v_cvt_pk_fp8_f32 v5, v9, v11 op_sel:[0,0,1]
	v_lshl_add_u64 v[6:7], s[6:7], 0, v[6:7]
	v_lshl_add_u64 v[6:7], v[6:7], 0, s[24:25]
	v_permlane16_swap_b32_e32 v2, v4
	v_permlane16_swap_b32_e32 v3, v5
	v_lshl_add_u64 v[6:7], v[6:7], 0, v[178:179]
	global_store_dwordx4 v[6:7], v[2:5], off
	v_pk_fma_f32 v[12:13], v[60:61], s[10:11], v[36:37] op_sel_hi:[1,0,1]
	v_pk_fma_f32 v[14:15], v[58:59], s[10:11], v[34:35] op_sel_hi:[1,0,1]
	v_pk_fma_f32 v[2:3], v[64:65], s[10:11], v[40:41] op_sel_hi:[1,0,1]
	v_pk_fma_f32 v[4:5], v[62:63], s[10:11], v[38:39] op_sel_hi:[1,0,1]
	v_pk_mul_f32 v[2:3], v[8:9], v[2:3] op_sel_hi:[0,1]
	v_pk_mul_f32 v[4:5], v[8:9], v[4:5] op_sel_hi:[0,1]
	v_pk_mul_f32 v[12:13], v[8:9], v[12:13] op_sel_hi:[0,1]
	v_pk_mul_f32 v[8:9], v[8:9], v[14:15] op_sel_hi:[0,1]
	v_med3_f32 v4, v4, s79, v189
	v_med3_f32 v5, v5, s79, v189
	v_med3_f32 v11, v2, s79, v189
	v_mov_b32_e32 v2, v179
	v_med3_f32 v14, v3, s79, v189
	v_cvt_pk_fp8_f32 v2, v4, v5
	v_med3_f32 v4, v8, s79, v189
	v_med3_f32 v5, v9, s79, v189
	v_mov_b32_e32 v3, v179
	v_cvt_pk_fp8_f32 v3, v4, v5
	v_med3_f32 v4, v12, s79, v189
	v_med3_f32 v5, v13, s79, v189
	v_pk_fma_f32 v[8:9], v[54:55], s[10:11], v[38:39] op_sel_hi:[1,0,1]
	v_cvt_pk_fp8_f32 v3, v4, v5 op_sel:[0,0,1]
	v_pk_fma_f32 v[4:5], v[56:57], s[10:11], v[40:41] op_sel_hi:[1,0,1]
	v_cvt_pk_fp8_f32 v2, v11, v14 op_sel:[0,0,1]
	v_pk_mul_f32 v[4:5], v[10:11], v[4:5] op_sel_hi:[0,1]
	v_pk_mul_f32 v[8:9], v[10:11], v[8:9] op_sel_hi:[0,1]
	v_pk_fma_f32 v[12:13], v[52:53], s[10:11], v[36:37] op_sel_hi:[1,0,1]
	v_pk_fma_f32 v[14:15], v[50:51], s[10:11], v[34:35] op_sel_hi:[1,0,1]
	v_pk_mul_f32 v[12:13], v[10:11], v[12:13] op_sel_hi:[0,1]
	v_pk_mul_f32 v[10:11], v[10:11], v[14:15] op_sel_hi:[0,1]
	v_med3_f32 v8, v8, s79, v189
	v_med3_f32 v9, v9, s79, v189
	v_med3_f32 v14, v4, s79, v189
	v_mov_b32_e32 v4, v179
	v_med3_f32 v15, v5, s79, v189
	v_cvt_pk_fp8_f32 v4, v8, v9
	v_med3_f32 v8, v10, s79, v189
	v_med3_f32 v9, v11, s79, v189
	v_mov_b32_e32 v5, v179
	v_cvt_pk_fp8_f32 v5, v8, v9
	v_med3_f32 v8, v12, s79, v189
	v_med3_f32 v9, v13, s79, v189
	v_cvt_pk_fp8_f32 v4, v14, v15 op_sel:[0,0,1]
	v_cvt_pk_fp8_f32 v5, v8, v9 op_sel:[0,0,1]
	s_andn2_b64 vcc, exec, s[0:1]
	s_mov_b64 s[0:1], -1
	v_permlane16_swap_b32_e32 v2, v4
	v_permlane16_swap_b32_e32 v3, v5
	v_readlane_b32 s38, v255, 28
	global_store_dwordx4 v[6:7], v[2:5], off offset:128
	s_cbranch_vccnz .LBB0_803
; #define PG8_BAR __builtin_amdgcn_s_barrier()
; template <class Epi, class Sched>
; __device__ __forceinline__ void gemm_phase(LAS unsigned char* lds, const Sched& S, const Epi& E) {
;     ...
;         cur = nxt; cA = nA; cB = nB; crot = nrot; ++ui;
;         E.prefetch(cur, epre);
;         if (wr == 1) PG8_BAR;
;     __device__ __forceinline__ void prefetch(const pg8::Unit& u, Pre& q) const {
;         int tz = threadIdx.x; asm volatile("" : "+v"(tz)); const int wid = tz >> 6, wr = wid >> 2, wc = wid & 3, fr = tz & 15, fq = (tz >> 4) & 3;
;         const int rl0 = wr * 64 + fr, col0 = u.pn * 256 + wc * 32 + 8 * fq;
;         const int mt = __builtin_amdgcn_readfirstlane(u.pm - tstart[u.e]);
;         const float* gp = sgate + (size_t)u.e * T + mt * 256;
; #pragma unroll
;         for (int bj = 0; bj < 2; ++bj)
; #pragma unroll
;             for (int n = 0; n < 2; ++n) q.bv[bj][n] = *(const f32x4*)(b_down + (size_t)u.e * D + col0 + bj * 128 + 4 * n);
; #pragma unroll
;         for (int ai = 0; ai < 2; ++ai)
; #pragma unroll
;             for (int m = 0; m < 4; ++m) q.gt[ai][m] = gp[rl0 + ai * 128 + m * 16];
;     }
	s_lshl_b32 s0, s96, 2
	s_add_i32 s0, s0, 0
	s_add_i32 s0, s0, 0x27d00
	v_mov_b32_e32 v4, v0
	v_mov_b32_e32 v2, s0
	ds_read_b32 v3, v2
	v_lshrrev_b32_e32 v2, 1, v4
	s_ashr_i32 s97, s96, 31
	v_readlane_b32 s16, v255, 29
	v_and_b32_e32 v2, 0x78, v2
	s_waitcnt lgkmcnt(0)
	v_sub_u32_e32 v3, s14, v3
	s_lshl_b64 s[0:1], s[96:97], 17
	v_readfirstlane_b32 s15, v3
	s_lshl_b32 s34, s15, 8
	s_ashr_i32 s35, s34, 31
	s_lshl_b64 s[36:37], s[96:97], 13
	v_readlane_b32 s26, v255, 39
	v_readlane_b32 s28, v255, 41
	v_lshl_or_b32 v2, s12, 8, v2
	v_readlane_b32 s27, v255, 40
	v_readlane_b32 s29, v255, 42
	s_add_u32 s26, s28, s36
	v_ashrrev_i32_e32 v3, 31, v2
	s_addc_u32 s27, s29, s37
	v_readlane_b32 s17, v255, 30
	v_lshl_add_u64 v[2:3], v[2:3], 2, s[26:27]
	s_add_u32 s15, s11, s0
	v_ashrrev_i32_e32 v5, 2, v4
	global_load_dwordx4 v[42:45], v[2:3], off offset:16
	global_load_dwordx4 v[46:49], v[2:3], off
	global_load_dwordx4 v[34:37], v[2:3], off offset:528
	global_load_dwordx4 v[38:41], v[2:3], off offset:512
	v_and_b32_e32 v2, 15, v4
	s_addc_u32 s17, s42, s1
	s_lshl_b64 s[0:1], s[34:35], 2
	v_and_or_b32 v2, v5, s91, v2
	s_add_u32 s0, s15, s0
	s_addc_u32 s1, s17, s1
	v_ashrrev_i32_e32 v3, 31, v2
	v_lshl_add_u64 v[2:3], v[2:3], 2, s[0:1]
	global_load_dword v197, v[2:3], off
	global_load_dword v196, v[2:3], off offset:64
	global_load_dword v195, v[2:3], off offset:128
	global_load_dword v194, v[2:3], off offset:192
	global_load_dword v193, v[2:3], off offset:512
	global_load_dword v192, v[2:3], off offset:576
	global_load_dword v191, v[2:3], off offset:640
	global_load_dword v190, v[2:3], off offset:704
	s_andn2_b64 vcc, exec, s[4:5]
	v_readlane_b32 s18, v255, 31
	v_readlane_b32 s19, v255, 32
	v_readlane_b32 s20, v255, 33
	v_readlane_b32 s21, v255, 34
	v_readlane_b32 s22, v255, 35
	v_readlane_b32 s23, v255, 36
	v_readlane_b32 s24, v255, 37
	v_readlane_b32 s25, v255, 38
	v_readlane_b32 s30, v255, 43
	v_readlane_b32 s31, v255, 44
	s_cbranch_vccnz .LBB0_802
	s_barrier
	s_branch .LBB0_802

; __global__ void __launch_bounds__(NTHREADS, 2) hymba_fwd(Params p) {
	.amdhsa_kernel _Z9hymba_fwd6Params
		.amdhsa_group_segment_fixed_size 0
		.amdhsa_private_segment_fixed_size 0
		.amdhsa_kernarg_size 472
		.amdhsa_user_sgpr_count 2
		.amdhsa_user_sgpr_dispatch_ptr 0
		.amdhsa_user_sgpr_queue_ptr 0
		.amdhsa_user_sgpr_kernarg_segment_ptr 1
		.amdhsa_user_sgpr_dispatch_id 0
		.amdhsa_user_sgpr_kernarg_preload_length 0
		.amdhsa_user_sgpr_kernarg_preload_offset 0
		.amdhsa_user_sgpr_private_segment_size 0
		.amdhsa_uses_dynamic_stack 0
		.amdhsa_enable_private_segment 0
		.amdhsa_system_sgpr_workgroup_id_x 1
		.amdhsa_system_sgpr_workgroup_id_y 0
		.amdhsa_system_sgpr_workgroup_id_z 0
		.amdhsa_system_sgpr_workgroup_info 0
		.amdhsa_system_vgpr_workitem_id 0
		.amdhsa_next_free_vgpr 256
		.amdhsa_next_free_sgpr 102
		.amdhsa_accum_offset 256
		.amdhsa_reserve_vcc 1
		.amdhsa_float_round_mode_32 0
		.amdhsa_float_round_mode_16_64 0
		.amdhsa_float_denorm_mode_32 3
		.amdhsa_float_denorm_mode_16_64 3
		.amdhsa_dx10_clamp 1
		.amdhsa_ieee_mode 1
		.amdhsa_fp16_overflow 0
		.amdhsa_tg_split 0
		.amdhsa_exception_fp_ieee_invalid_op 0
		.amdhsa_exception_fp_denorm_src 0
		.amdhsa_exception_fp_ieee_div_zero 0
		.amdhsa_exception_fp_ieee_overflow 0
		.amdhsa_exception_fp_ieee_underflow 0
		.amdhsa_exception_fp_ieee_inexact 0
		.amdhsa_exception_int_div_zero 0
	.end_amdhsa_kernel

; __global__ void __launch_bounds__(NTHREADS, 2) hymba_fwd(Params p) {
amdhsa.kernels:
  - .agpr_count:     0
    .args:
      - .offset:         0
        .size:           216
        .value_kind:     by_value
      - .offset:         216
        .size:           4
        .value_kind:     hidden_block_count_x
      - .offset:         220
        .size:           4
        .value_kind:     hidden_block_count_y
      - .offset:         224
        .size:           4
        .value_kind:     hidden_block_count_z
      - .offset:         228
        .size:           2
        .value_kind:     hidden_group_size_x
      - .offset:         230
        .size:           2
        .value_kind:     hidden_group_size_y
      - .offset:         232
        .size:           2
        .value_kind:     hidden_group_size_z
      - .offset:         234
        .size:           2
        .value_kind:     hidden_remainder_x
      - .offset:         236
        .size:           2
        .value_kind:     hidden_remainder_y
      - .offset:         238
        .size:           2
        .value_kind:     hidden_remainder_z
      - .offset:         256
        .size:           8
        .value_kind:     hidden_global_offset_x
      - .offset:         264
        .size:           8
        .value_kind:     hidden_global_offset_y
      - .offset:         272
        .size:           8
        .value_kind:     hidden_global_offset_z
      - .offset:         280
        .size:           2
        .value_kind:     hidden_grid_dims
      - .offset:         336
        .size:           4
        .value_kind:     hidden_dynamic_lds_size
    .group_segment_fixed_size: 0
    .kernarg_segment_align: 8
    .kernarg_segment_size: 472
    .language:       OpenCL C
    .language_version:
      - 2
      - 0
    .max_flat_workgroup_size: 512
    .name:           _Z9hymba_fwd6Params
    .private_segment_fixed_size: 0
    .sgpr_count:     108
    .sgpr_spill_count: 69
    .symbol:         _Z9hymba_fwd6Params.kd
    .uniform_work_group_size: 1
    .uses_dynamic_stack: false
    .vgpr_count:     256
    .vgpr_spill_count: 0
    .wavefront_size: 64
